# mix GEMM mid hook: second half gate-logit loads hoisted beside the first half loads (one exposed latency less), on top of the unit-boundary barrier edit
# baseline (speedup 1.0000x reference)
.LBB0_1046:
	ds_read_b128 v[136:139], v172
	ds_read_b128 v[140:143], v172 offset:1024
	ds_read_b128 v[144:147], v172 offset:2048
	ds_read_b128 v[148:151], v172 offset:3072
	ds_read_b128 v[152:155], v173
	ds_read_b128 v[156:159], v173 offset:1024
	ds_read_b128 v[160:163], v173 offset:2048
	ds_read_b128 v[178:181], v173 offset:3072
	s_add_u32 s25, s64, s56
	s_addc_u32 s33, s65, s57
	s_add_u32 s66, s25, 0x100
	s_addc_u32 s67, s33, 0
	s_add_u32 s23, s62, s56
	s_addc_u32 s24, s63, s57
	s_add_u32 s28, s23, 0x100
	s_addc_u32 s29, s24, 0
	s_add_u32 s58, s25, 0x180
	s_addc_u32 s59, s33, 0
	ds_read_b128 v[182:185], v174
	ds_read_b128 v[186:189], v174 offset:1024
	ds_read_b128 v[190:193], v174 offset:2048
	ds_read_b128 v[194:197], v174 offset:3072
	ds_read_b128 v[198:201], v174 offset:4096
	ds_read_b128 v[202:205], v174 offset:5120
	ds_read_b128 v[206:209], v174 offset:6144
	ds_read_b128 v[210:213], v174 offset:7168
	s_add_u32 s30, s25, 0x40080
	s_addc_u32 s31, s33, 0
	s_mov_b32 s36, m0
	s_mov_b32 m0, s26
	s_nop 2
	global_load_lds_dwordx4 v165, s[30:31]
	s_mov_b32 m0, s36
	s_nop 0
	s_mov_b32 s36, m0
	s_mov_b32 m0, s27
	s_nop 2
	global_load_lds_dwordx4 v167, s[30:31]
	s_mov_b32 m0, s36
	s_waitcnt vmcnt(8)
	s_waitcnt lgkmcnt(0)
	s_barrier
	s_setprio 1
	s_waitcnt lgkmcnt(7)
	v_mfma_f32_16x16x32_bf16 v[26:29], v[136:139], v[182:185], v[26:29]
	v_mfma_f32_16x16x32_bf16 v[30:33], v[144:147], v[182:185], v[30:33]
	s_waitcnt lgkmcnt(5)
	v_mfma_f32_16x16x32_bf16 v[50:53], v[136:139], v[190:193], v[50:53]
	v_mfma_f32_16x16x32_bf16 v[54:57], v[144:147], v[190:193], v[54:57]
	s_waitcnt lgkmcnt(3)
	v_mfma_f32_16x16x32_bf16 v[74:77], v[136:139], v[198:201], v[74:77]
	v_mfma_f32_16x16x32_bf16 v[78:81], v[144:147], v[198:201], v[78:81]
	s_waitcnt lgkmcnt(1)
	v_mfma_f32_16x16x32_bf16 v[94:97], v[136:139], v[206:209], v[94:97]
	v_mfma_f32_16x16x32_bf16 v[102:105], v[144:147], v[206:209], v[102:105]
	v_mfma_f32_16x16x32_bf16 v[26:29], v[140:143], v[186:189], v[26:29]
	v_mfma_f32_16x16x32_bf16 v[30:33], v[148:151], v[186:189], v[30:33]
	v_mfma_f32_16x16x32_bf16 v[50:53], v[140:143], v[194:197], v[50:53]
	v_mfma_f32_16x16x32_bf16 v[54:57], v[148:151], v[194:197], v[54:57]
	v_mfma_f32_16x16x32_bf16 v[74:77], v[140:143], v[202:205], v[74:77]
	v_mfma_f32_16x16x32_bf16 v[78:81], v[148:151], v[202:205], v[78:81]
	s_waitcnt lgkmcnt(0)
	v_mfma_f32_16x16x32_bf16 v[94:97], v[140:143], v[210:213], v[94:97]
	v_mfma_f32_16x16x32_bf16 v[102:105], v[148:151], v[210:213], v[102:105]
	s_setprio 0
	s_setprio 1
	v_mfma_f32_16x16x32_bf16 v[38:41], v[152:155], v[182:185], v[38:41]
	v_mfma_f32_16x16x32_bf16 v[42:45], v[160:163], v[182:185], v[42:45]
	v_mfma_f32_16x16x32_bf16 v[62:65], v[152:155], v[190:193], v[62:65]
	v_mfma_f32_16x16x32_bf16 v[66:69], v[160:163], v[190:193], v[66:69]
	v_mfma_f32_16x16x32_bf16 v[82:85], v[152:155], v[198:201], v[82:85]
	v_mfma_f32_16x16x32_bf16 v[90:93], v[160:163], v[198:201], v[90:93]
	v_mfma_f32_16x16x32_bf16 v[106:109], v[152:155], v[206:209], v[106:109]
	v_mfma_f32_16x16x32_bf16 v[114:117], v[160:163], v[206:209], v[114:117]
	v_mfma_f32_16x16x32_bf16 v[38:41], v[156:159], v[186:189], v[38:41]
	v_mfma_f32_16x16x32_bf16 v[42:45], v[178:181], v[186:189], v[42:45]
	v_mfma_f32_16x16x32_bf16 v[62:65], v[156:159], v[194:197], v[62:65]
	v_mfma_f32_16x16x32_bf16 v[66:69], v[178:181], v[194:197], v[66:69]
	v_mfma_f32_16x16x32_bf16 v[82:85], v[156:159], v[202:205], v[82:85]
	v_mfma_f32_16x16x32_bf16 v[90:93], v[178:181], v[202:205], v[90:93]
	v_mfma_f32_16x16x32_bf16 v[106:109], v[156:159], v[210:213], v[106:109]
	v_mfma_f32_16x16x32_bf16 v[114:117], v[178:181], v[210:213], v[114:117]
	s_setprio 0
	s_barrier
	ds_read_b128 v[182:185], v174 offset:16384
	ds_read_b128 v[186:189], v174 offset:17408
	ds_read_b128 v[190:193], v174 offset:18432
	ds_read_b128 v[194:197], v174 offset:19456
	ds_read_b128 v[198:201], v174 offset:20480
	ds_read_b128 v[202:205], v174 offset:21504
	ds_read_b128 v[206:209], v174 offset:22528
	ds_read_b128 v[210:213], v174 offset:23552
	s_mov_b32 s30, m0
	s_mov_b32 m0, s80
	s_nop 2
	global_load_lds_dwordx4 v166, s[28:29]
	s_mov_b32 m0, s30
	s_nop 0
	s_mov_b32 s30, m0
	s_mov_b32 m0, s81
	s_nop 2
	global_load_lds_dwordx4 v168, s[28:29]
	s_mov_b32 m0, s30
	s_add_u32 s28, s23, 0x40100
	s_addc_u32 s29, s24, 0
	s_mov_b32 s30, m0
	s_mov_b32 m0, s82
	s_nop 2
	global_load_lds_dwordx4 v166, s[28:29]
	s_mov_b32 m0, s30
	s_nop 0
	s_mov_b32 s30, m0
	s_mov_b32 m0, s83
	s_nop 2
	global_load_lds_dwordx4 v168, s[28:29]
	s_mov_b32 m0, s30
	s_mov_b32 s28, m0
	s_mov_b32 m0, s79
	s_nop 2
	global_load_lds_dwordx4 v165, s[66:67]
	s_mov_b32 m0, s28
	s_nop 0
	s_mov_b32 s28, m0
	s_mov_b32 m0, s84
	s_nop 2
	global_load_lds_dwordx4 v167, s[66:67]
	s_mov_b32 m0, s28
	s_waitcnt vmcnt(8)
	s_waitcnt lgkmcnt(0)
	s_barrier
	s_setprio 1
	s_waitcnt lgkmcnt(7)
	v_mfma_f32_16x16x32_bf16 v[118:121], v[136:139], v[182:185], v[118:121]
	v_mfma_f32_16x16x32_bf16 v[126:129], v[144:147], v[182:185], v[126:129]
	s_waitcnt lgkmcnt(5)
	v_mfma_f32_16x16x32_bf16 v[98:101], v[136:139], v[190:193], v[98:101]
	v_mfma_f32_16x16x32_bf16 v[86:89], v[144:147], v[190:193], v[86:89]
	s_waitcnt lgkmcnt(3)
	v_mfma_f32_16x16x32_bf16 v[46:49], v[136:139], v[198:201], v[46:49]
	v_mfma_f32_16x16x32_bf16 v[34:37], v[144:147], v[198:201], v[34:37]
	s_waitcnt lgkmcnt(1)
	v_mfma_f32_16x16x32_bf16 v[14:17], v[136:139], v[206:209], v[14:17]
	v_mfma_f32_16x16x32_bf16 v[10:13], v[144:147], v[206:209], v[10:13]
	v_mfma_f32_16x16x32_bf16 v[118:121], v[140:143], v[186:189], v[118:121]
	v_mfma_f32_16x16x32_bf16 v[126:129], v[148:151], v[186:189], v[126:129]
	v_mfma_f32_16x16x32_bf16 v[98:101], v[140:143], v[194:197], v[98:101]
	v_mfma_f32_16x16x32_bf16 v[86:89], v[148:151], v[194:197], v[86:89]
	v_mfma_f32_16x16x32_bf16 v[46:49], v[140:143], v[202:205], v[46:49]
	v_mfma_f32_16x16x32_bf16 v[34:37], v[148:151], v[202:205], v[34:37]
	s_waitcnt lgkmcnt(0)
	v_mfma_f32_16x16x32_bf16 v[14:17], v[140:143], v[210:213], v[14:17]
	v_mfma_f32_16x16x32_bf16 v[10:13], v[148:151], v[210:213], v[10:13]
	s_setprio 0
	s_setprio 1
	v_mfma_f32_16x16x32_bf16 v[122:125], v[152:155], v[182:185], v[122:125]
	v_mfma_f32_16x16x32_bf16 v[110:113], v[160:163], v[182:185], v[110:113]
	v_mfma_f32_16x16x32_bf16 v[70:73], v[152:155], v[190:193], v[70:73]
	v_mfma_f32_16x16x32_bf16 v[58:61], v[160:163], v[190:193], v[58:61]
	v_mfma_f32_16x16x32_bf16 v[22:25], v[152:155], v[198:201], v[22:25]
	v_mfma_f32_16x16x32_bf16 v[18:21], v[160:163], v[198:201], v[18:21]
	v_mfma_f32_16x16x32_bf16 v[6:9], v[152:155], v[206:209], v[6:9]
	v_mfma_f32_16x16x32_bf16 v[2:5], v[160:163], v[206:209], v[2:5]
	v_mfma_f32_16x16x32_bf16 v[122:125], v[156:159], v[186:189], v[122:125]
	v_mfma_f32_16x16x32_bf16 v[110:113], v[178:181], v[186:189], v[110:113]
	v_mfma_f32_16x16x32_bf16 v[70:73], v[156:159], v[194:197], v[70:73]
	v_mfma_f32_16x16x32_bf16 v[58:61], v[178:181], v[194:197], v[58:61]
	v_mfma_f32_16x16x32_bf16 v[22:25], v[156:159], v[202:205], v[22:25]
	v_mfma_f32_16x16x32_bf16 v[18:21], v[178:181], v[202:205], v[18:21]
	v_mfma_f32_16x16x32_bf16 v[6:9], v[156:159], v[210:213], v[6:9]
	v_mfma_f32_16x16x32_bf16 v[2:5], v[178:181], v[210:213], v[2:5]
	s_setprio 0
	s_barrier
	ds_read_b128 v[136:139], v175
	ds_read_b128 v[140:143], v175 offset:1024
	ds_read_b128 v[144:147], v175 offset:2048
	ds_read_b128 v[148:151], v175 offset:3072
	ds_read_b128 v[152:155], v176
	ds_read_b128 v[156:159], v176 offset:1024
	ds_read_b128 v[160:163], v176 offset:2048
	ds_read_b128 v[178:181], v176 offset:3072
	ds_read_b128 v[182:185], v174 offset:32768
	ds_read_b128 v[186:189], v174 offset:33792
	ds_read_b128 v[190:193], v174 offset:34816
	ds_read_b128 v[194:197], v174 offset:35840
	ds_read_b128 v[198:201], v174 offset:36864
	ds_read_b128 v[202:205], v174 offset:37888
	ds_read_b128 v[206:209], v174 offset:38912
	ds_read_b128 v[210:213], v174 offset:39936
	s_add_u32 s28, s25, 0x40100
	s_addc_u32 s29, s33, 0
	s_mov_b32 s25, m0
	s_mov_b32 m0, s85
	s_nop 2
	global_load_lds_dwordx4 v165, s[28:29]
	s_mov_b32 m0, s25
	s_nop 0
	s_mov_b32 s25, m0
	s_mov_b32 m0, s86
	s_nop 2
	global_load_lds_dwordx4 v167, s[28:29]
	s_mov_b32 m0, s25
	s_waitcnt vmcnt(8)
	s_waitcnt lgkmcnt(0)
	s_barrier
	s_setprio 1
	s_waitcnt lgkmcnt(7)
	v_mfma_f32_16x16x32_bf16 v[26:29], v[136:139], v[182:185], v[26:29]
	v_mfma_f32_16x16x32_bf16 v[30:33], v[144:147], v[182:185], v[30:33]
	s_waitcnt lgkmcnt(5)
	v_mfma_f32_16x16x32_bf16 v[50:53], v[136:139], v[190:193], v[50:53]
	v_mfma_f32_16x16x32_bf16 v[54:57], v[144:147], v[190:193], v[54:57]
	s_waitcnt lgkmcnt(3)
	v_mfma_f32_16x16x32_bf16 v[74:77], v[136:139], v[198:201], v[74:77]
	v_mfma_f32_16x16x32_bf16 v[78:81], v[144:147], v[198:201], v[78:81]
	s_waitcnt lgkmcnt(1)
	v_mfma_f32_16x16x32_bf16 v[94:97], v[136:139], v[206:209], v[94:97]
	v_mfma_f32_16x16x32_bf16 v[102:105], v[144:147], v[206:209], v[102:105]
	v_mfma_f32_16x16x32_bf16 v[26:29], v[140:143], v[186:189], v[26:29]
	v_mfma_f32_16x16x32_bf16 v[30:33], v[148:151], v[186:189], v[30:33]
	v_mfma_f32_16x16x32_bf16 v[50:53], v[140:143], v[194:197], v[50:53]
	v_mfma_f32_16x16x32_bf16 v[54:57], v[148:151], v[194:197], v[54:57]
	v_mfma_f32_16x16x32_bf16 v[74:77], v[140:143], v[202:205], v[74:77]
	v_mfma_f32_16x16x32_bf16 v[78:81], v[148:151], v[202:205], v[78:81]
	s_waitcnt lgkmcnt(0)
	v_mfma_f32_16x16x32_bf16 v[94:97], v[140:143], v[210:213], v[94:97]
	v_mfma_f32_16x16x32_bf16 v[102:105], v[148:151], v[210:213], v[102:105]
	s_setprio 0
	s_setprio 1
	v_mfma_f32_16x16x32_bf16 v[38:41], v[152:155], v[182:185], v[38:41]
	v_mfma_f32_16x16x32_bf16 v[42:45], v[160:163], v[182:185], v[42:45]
	v_mfma_f32_16x16x32_bf16 v[62:65], v[152:155], v[190:193], v[62:65]
	v_mfma_f32_16x16x32_bf16 v[66:69], v[160:163], v[190:193], v[66:69]
	v_mfma_f32_16x16x32_bf16 v[82:85], v[152:155], v[198:201], v[82:85]
	v_mfma_f32_16x16x32_bf16 v[90:93], v[160:163], v[198:201], v[90:93]
	v_mfma_f32_16x16x32_bf16 v[106:109], v[152:155], v[206:209], v[106:109]
	v_mfma_f32_16x16x32_bf16 v[114:117], v[160:163], v[206:209], v[114:117]
	v_mfma_f32_16x16x32_bf16 v[38:41], v[156:159], v[186:189], v[38:41]
	v_mfma_f32_16x16x32_bf16 v[42:45], v[178:181], v[186:189], v[42:45]
	v_mfma_f32_16x16x32_bf16 v[62:65], v[156:159], v[194:197], v[62:65]
	v_mfma_f32_16x16x32_bf16 v[66:69], v[178:181], v[194:197], v[66:69]
	v_mfma_f32_16x16x32_bf16 v[82:85], v[156:159], v[202:205], v[82:85]
	v_mfma_f32_16x16x32_bf16 v[90:93], v[178:181], v[202:205], v[90:93]
	v_mfma_f32_16x16x32_bf16 v[106:109], v[156:159], v[210:213], v[106:109]
	v_mfma_f32_16x16x32_bf16 v[114:117], v[178:181], v[210:213], v[114:117]
	s_setprio 0
	s_barrier
	ds_read_b128 v[182:185], v174 offset:49152
	ds_read_b128 v[186:189], v174 offset:50176
	ds_read_b128 v[190:193], v174 offset:51200
	ds_read_b128 v[194:197], v174 offset:52224
	ds_read_b128 v[198:201], v174 offset:53248
	ds_read_b128 v[202:205], v174 offset:54272
	ds_read_b128 v[206:209], v174 offset:55296
	ds_read_b128 v[210:213], v174 offset:56320
	s_add_u32 s28, s23, 0x180
	s_addc_u32 s29, s24, 0
	s_mov_b32 s25, m0
	s_mov_b32 m0, s92
	s_nop 2
	global_load_lds_dwordx4 v166, s[28:29]
	s_mov_b32 m0, s25
	s_nop 0
	s_mov_b32 s25, m0
	s_mov_b32 m0, s93
	s_nop 2
	global_load_lds_dwordx4 v168, s[28:29]
	s_mov_b32 m0, s25
	s_add_u32 s28, s23, 0x40180
	s_addc_u32 s29, s24, 0
	s_mov_b32 s23, m0
	s_mov_b32 m0, s96
	s_nop 2
	global_load_lds_dwordx4 v166, s[28:29]
	s_mov_b32 m0, s23
	s_nop 0
	s_mov_b32 s23, m0
	s_mov_b32 m0, s97
	s_nop 2
	global_load_lds_dwordx4 v168, s[28:29]
	s_mov_b32 m0, s23
	s_nop 0
	s_mov_b32 s23, m0
	s_mov_b32 m0, s94
	s_nop 2
	global_load_lds_dwordx4 v165, s[58:59]
	s_mov_b32 m0, s23
	s_nop 0
	s_mov_b32 s23, m0
	s_mov_b32 m0, s95
	s_nop 2
	global_load_lds_dwordx4 v167, s[58:59]
	s_mov_b32 m0, s23
	s_waitcnt vmcnt(8)
	s_waitcnt lgkmcnt(0)
	s_barrier
	s_setprio 1
	s_waitcnt lgkmcnt(7)
	v_mfma_f32_16x16x32_bf16 v[118:121], v[136:139], v[182:185], v[118:121]
	v_mfma_f32_16x16x32_bf16 v[126:129], v[144:147], v[182:185], v[126:129]
	s_waitcnt lgkmcnt(5)
	v_mfma_f32_16x16x32_bf16 v[98:101], v[136:139], v[190:193], v[98:101]
	v_mfma_f32_16x16x32_bf16 v[86:89], v[144:147], v[190:193], v[86:89]
	s_waitcnt lgkmcnt(3)
	v_mfma_f32_16x16x32_bf16 v[46:49], v[136:139], v[198:201], v[46:49]
	v_mfma_f32_16x16x32_bf16 v[34:37], v[144:147], v[198:201], v[34:37]
	s_waitcnt lgkmcnt(1)
	v_mfma_f32_16x16x32_bf16 v[14:17], v[136:139], v[206:209], v[14:17]
	v_mfma_f32_16x16x32_bf16 v[10:13], v[144:147], v[206:209], v[10:13]
	v_mfma_f32_16x16x32_bf16 v[118:121], v[140:143], v[186:189], v[118:121]
	v_mfma_f32_16x16x32_bf16 v[126:129], v[148:151], v[186:189], v[126:129]
	v_mfma_f32_16x16x32_bf16 v[98:101], v[140:143], v[194:197], v[98:101]
	v_mfma_f32_16x16x32_bf16 v[86:89], v[148:151], v[194:197], v[86:89]
	v_mfma_f32_16x16x32_bf16 v[46:49], v[140:143], v[202:205], v[46:49]
	v_mfma_f32_16x16x32_bf16 v[34:37], v[148:151], v[202:205], v[34:37]
	s_waitcnt lgkmcnt(0)
	v_mfma_f32_16x16x32_bf16 v[14:17], v[140:143], v[210:213], v[14:17]
	v_mfma_f32_16x16x32_bf16 v[10:13], v[148:151], v[210:213], v[10:13]
	s_setprio 0
	s_setprio 1
	v_mfma_f32_16x16x32_bf16 v[122:125], v[152:155], v[182:185], v[122:125]
	v_mfma_f32_16x16x32_bf16 v[110:113], v[160:163], v[182:185], v[110:113]
	v_mfma_f32_16x16x32_bf16 v[70:73], v[152:155], v[190:193], v[70:73]
	v_mfma_f32_16x16x32_bf16 v[58:61], v[160:163], v[190:193], v[58:61]
	v_mfma_f32_16x16x32_bf16 v[22:25], v[152:155], v[198:201], v[22:25]
	v_mfma_f32_16x16x32_bf16 v[18:21], v[160:163], v[198:201], v[18:21]
	v_mfma_f32_16x16x32_bf16 v[6:9], v[152:155], v[206:209], v[6:9]
	v_mfma_f32_16x16x32_bf16 v[2:5], v[160:163], v[206:209], v[2:5]
	v_mfma_f32_16x16x32_bf16 v[122:125], v[156:159], v[186:189], v[122:125]
	v_mfma_f32_16x16x32_bf16 v[110:113], v[178:181], v[186:189], v[110:113]
	v_mfma_f32_16x16x32_bf16 v[70:73], v[156:159], v[194:197], v[70:73]
	v_mfma_f32_16x16x32_bf16 v[58:61], v[178:181], v[194:197], v[58:61]
	v_mfma_f32_16x16x32_bf16 v[22:25], v[156:159], v[202:205], v[22:25]
	v_mfma_f32_16x16x32_bf16 v[18:21], v[178:181], v[202:205], v[18:21]
	v_mfma_f32_16x16x32_bf16 v[6:9], v[156:159], v[210:213], v[6:9]
	v_mfma_f32_16x16x32_bf16 v[2:5], v[178:181], v[210:213], v[2:5]
	s_setprio 0
	s_barrier
	s_add_i32 s3, s3, 2
	s_add_u32 s56, s56, 0x100
	s_addc_u32 s57, s57, 0
	s_cmp_gt_u32 s3, 5
	s_cbranch_scc0 .LBB0_1046
	s_ashr_i32 s55, s54, 31
	s_lshl_b64 s[24:25], s[54:55], 19
	s_add_u32 s56, s69, s24
	s_addc_u32 s57, s76, s25
	s_ashr_i32 s23, s22, 31
	s_lshl_b64 s[24:25], s[22:23], 19
	s_add_u32 s58, s77, s24
	s_addc_u32 s59, s78, s25
	s_lshl_b32 s3, s60, 18
	s_lshl_b32 s23, s2, 8
	s_add_i32 s2, s23, s3
	v_add_u32_e32 v134, s2, v171
	global_load_dwordx2 v[162:163], v134, s[14:15]
	global_load_dwordx2 v[178:179], v134, s[16:17]
	v_or_b32_e32 v136, 0x80, v134
	v_add_u32_e32 v137, 0x4000, v134
	v_add_u32_e32 v138, 0x4080, v134
	v_add_u32_e32 v139, 0x8000, v134
	v_add_u32_e32 v140, 0x8080, v134
	v_add_u32_e32 v141, 0xc000, v134
	v_add_u32_e32 v161, 0xc080, v134
	global_load_dwordx2 v[180:181], v136, s[14:15]
	global_load_dwordx2 v[182:183], v136, s[16:17]
	global_load_dwordx2 v[158:159], v137, s[14:15]
	global_load_dwordx2 v[156:157], v137, s[16:17]
	global_load_dwordx2 v[154:155], v138, s[14:15]
	global_load_dwordx2 v[152:153], v138, s[16:17]
	global_load_dwordx2 v[150:151], v139, s[14:15]
	global_load_dwordx2 v[148:149], v139, s[16:17]
	global_load_dwordx2 v[146:147], v140, s[14:15]
	global_load_dwordx2 v[144:145], v140, s[16:17]
	global_load_dwordx2 v[142:143], v141, s[14:15]
	s_nop 0
	global_load_dwordx2 v[140:141], v141, s[16:17]
	s_nop 0
	global_load_dwordx2 v[138:139], v161, s[14:15]
	global_load_dwordx2 v[136:137], v161, s[16:17]
	v_add_u32_e32 v160, 0x20000, v134
	global_load_dwordx2 v[220:221], v160, s[14:15]
	global_load_dwordx2 v[222:223], v160, s[16:17]
	v_add_u32_e32 v214, 0x20080, v134
	v_add_u32_e32 v215, 0x24000, v134
	v_add_u32_e32 v216, 0x24080, v134
	v_add_u32_e32 v217, 0x28000, v134
	global_load_dwordx2 v[224:225], v214, s[14:15]
	global_load_dwordx2 v[226:227], v214, s[16:17]
	global_load_dwordx2 v[228:229], v215, s[14:15]
	global_load_dwordx2 v[230:231], v215, s[16:17]
	global_load_dwordx2 v[232:233], v216, s[14:15]
	global_load_dwordx2 v[234:235], v216, s[16:17]
	global_load_dwordx2 v[236:237], v217, s[14:15]
	global_load_dwordx2 v[238:239], v217, s[16:17]
	v_add_u32_e32 v214, 0x28080, v134
	v_add_u32_e32 v215, 0x2c000, v134
	v_add_u32_e32 v216, 0x2c080, v134
	global_load_dwordx2 v[240:241], v214, s[14:15]
	global_load_dwordx2 v[242:243], v214, s[16:17]
	global_load_dwordx2 v[244:245], v215, s[14:15]
	global_load_dwordx2 v[246:247], v215, s[16:17]
	global_load_dwordx2 v[248:249], v216, s[14:15]
	global_load_dwordx2 v[250:251], v216, s[16:17]
	s_and_b64 s[2:3], s[4:5], exec
	s_cselect_b32 s2, s57, s65
	s_cselect_b32 s3, s56, s64
	s_cselect_b32 s24, s59, s63
	s_cselect_b32 s25, s58, s62
	s_add_u32 s28, s64, 0x500
	s_addc_u32 s29, s65, 0
	s_add_u32 s30, s62, 0x500
	s_addc_u32 s31, s63, 0
	s_mov_b32 s33, 6
	s_waitcnt vmcnt(31)
	v_cvt_pk_f32_fp8_e32 v[184:185], v162
	s_waitcnt vmcnt(30)
	v_cvt_pk_f32_fp8_e32 v[190:191], v178
	v_cvt_pk_f32_fp8_e32 v[188:189], v163
	v_cvt_pk_f32_fp8_sdwa v[192:193], v178 src0_sel:WORD_1
	v_cvt_pk_f32_fp8_e32 v[194:195], v179
	v_max_f32_e32 v161, v190, v190
	v_max_f32_e32 v184, v184, v184
	v_max_f32_e32 v190, v191, v191
	v_max_f32_e32 v185, v185, v185
	v_max_f32_e32 v188, v188, v188
	v_med3_f32 v161, v161, s35, v177
	v_med3_f32 v184, v184, s35, v177
	v_max_f32_e32 v191, v192, v192
	v_max_f32_e32 v192, v193, v193
	v_max_f32_e32 v193, v194, v194
	v_max_f32_e32 v194, v195, v195
	v_max_f32_e32 v189, v189, v189
	v_med3_f32 v190, v190, s35, v177
	v_med3_f32 v185, v185, s35, v177
	v_med3_f32 v188, v188, s35, v177
	v_mul_f32_e32 v161, 0xbfb8aa3b, v161
	v_mul_f32_e32 v195, 0xbfb8aa3b, v184
	v_cvt_pk_f32_fp8_sdwa v[186:187], v162 src0_sel:WORD_1
	v_cvt_pk_f32_fp8_sdwa v[162:163], v163 src0_sel:WORD_1
	v_med3_f32 v194, v194, s35, v177
	v_med3_f32 v189, v189, s35, v177
	v_mul_f32_e32 v190, 0xbfb8aa3b, v190
	v_mul_f32_e32 v196, 0xbfb8aa3b, v185
	v_mul_f32_e32 v199, 0xbfb8aa3b, v188
	v_exp_f32_e32 v184, v161
	v_exp_f32_e32 v161, v195
	v_mul_f32_e32 v200, 0xbfb8aa3b, v194
	v_mul_f32_e32 v189, 0xbfb8aa3b, v189
	v_exp_f32_e32 v185, v190
	v_exp_f32_e32 v190, v196
	v_exp_f32_e32 v194, v199
	v_exp_f32_e32 v195, v189
	v_cvt_pk_f32_fp8_sdwa v[178:179], v179 src0_sel:WORD_1
	v_add_f32_e32 v161, 1.0, v161
	v_max_f32_e32 v162, v162, v162
	v_add_f32_e32 v189, 1.0, v190
	v_rcp_f32_e32 v190, v161
	v_add_f32_e32 v161, 1.0, v194
	v_med3_f32 v162, v162, s35, v177
	v_rcp_f32_e32 v194, v161
	v_add_f32_e32 v161, 1.0, v195
	v_mul_f32_e32 v162, 0xbfb8aa3b, v162
	v_rcp_f32_e32 v195, v161
	v_max_f32_e32 v161, v178, v178
	v_exp_f32_e32 v178, v162
	v_max_f32_e32 v163, v163, v163
	v_med3_f32 v161, v161, s35, v177
	v_med3_f32 v163, v163, s35, v177
	v_mul_f32_e32 v161, 0xbfb8aa3b, v161
	v_mul_f32_e32 v163, 0xbfb8aa3b, v163
	v_max_f32_e32 v186, v186, v186
	v_max_f32_e32 v187, v187, v187
	v_exp_f32_e32 v162, v161
	v_add_f32_e32 v161, 1.0, v178
	v_max_f32_e32 v178, v179, v179
	v_exp_f32_e32 v179, v163
	v_med3_f32 v191, v191, s35, v177
	v_med3_f32 v186, v186, s35, v177
	v_med3_f32 v192, v192, s35, v177
	v_med3_f32 v187, v187, s35, v177
	v_mul_f32_e32 v191, 0xbfb8aa3b, v191
	v_mul_f32_e32 v197, 0xbfb8aa3b, v186
	v_mul_f32_e32 v192, 0xbfb8aa3b, v192
	v_mul_f32_e32 v198, 0xbfb8aa3b, v187
	v_med3_f32 v178, v178, s35, v177
	v_exp_f32_e32 v186, v191
	v_exp_f32_e32 v191, v197
	v_exp_f32_e32 v187, v192
	v_exp_f32_e32 v192, v198
	v_mul_f32_e32 v163, 0xbfb8aa3b, v178
	v_exp_f32_e32 v163, v163
	v_rcp_f32_e32 v178, v161
	v_add_f32_e32 v161, 1.0, v179
	v_med3_f32 v193, v193, s35, v177
	v_rcp_f32_e32 v179, v161
	v_mul_f32_e32 v193, 0xbfb8aa3b, v193
	v_exp_f32_e32 v188, v193
	v_add_f32_e32 v193, 1.0, v191
	v_add_f32_e32 v196, 1.0, v192
	v_rcp_f32_e32 v192, v193
	v_rcp_f32_e32 v193, v196
	v_pk_add_f32 v[162:163], v[162:163], 1.0 op_sel_hi:[1,0]
	v_pk_add_f32 v[186:187], v[186:187], 1.0 op_sel_hi:[1,0]
	v_pk_mul_f32 v[162:163], v[178:179], v[162:163]
	v_pk_mul_f32 v[186:187], v[192:193], v[186:187]
	v_pk_mul_f32 v[32:33], v[32:33], v[162:163]
	s_waitcnt vmcnt(29)
	v_cvt_pk_f32_fp8_e32 v[162:163], v180
	v_pk_mul_f32 v[28:29], v[28:29], v[186:187]
	s_waitcnt vmcnt(28)
	v_cvt_pk_f32_fp8_e32 v[186:187], v182
	v_rcp_f32_e32 v191, v189
	v_max_f32_e32 v162, v162, v162
	v_med3_f32 v162, v162, s35, v177
	v_mul_f32_e32 v162, 0xbfb8aa3b, v162
	v_max_f32_e32 v161, v186, v186
	v_exp_f32_e32 v186, v162
	v_exp_f32_e32 v189, v200
	v_med3_f32 v161, v161, s35, v177
	v_max_f32_e32 v163, v163, v163
	v_cvt_pk_f32_fp8_sdwa v[178:179], v180 src0_sel:WORD_1
	v_mul_f32_e32 v161, 0xbfb8aa3b, v161
	v_med3_f32 v163, v163, s35, v177
	v_pk_add_f32 v[184:185], v[184:185], 1.0 op_sel_hi:[1,0]
	v_exp_f32_e32 v162, v161
	v_add_f32_e32 v161, 1.0, v186
	v_mul_f32_e32 v163, 0xbfb8aa3b, v163
	v_pk_mul_f32 v[184:185], v[190:191], v[184:185]
	v_rcp_f32_e32 v186, v161
	v_max_f32_e32 v161, v187, v187
	v_exp_f32_e32 v187, v163
	v_pk_mul_f32 v[26:27], v[26:27], v[184:185]
	v_pk_add_f32 v[184:185], v[188:189], 1.0 op_sel_hi:[1,0]
	v_cvt_pk_f32_fp8_sdwa v[188:189], v182 src0_sel:WORD_1
	v_med3_f32 v161, v161, s35, v177
	v_max_f32_e32 v178, v178, v178
	v_mul_f32_e32 v161, 0xbfb8aa3b, v161
	v_med3_f32 v178, v178, s35, v177
	v_exp_f32_e32 v163, v161
	v_add_f32_e32 v161, 1.0, v187
	v_mul_f32_e32 v178, 0xbfb8aa3b, v178
	v_pk_mul_f32 v[184:185], v[194:195], v[184:185]
	v_rcp_f32_e32 v187, v161
	v_max_f32_e32 v161, v188, v188
	v_exp_f32_e32 v188, v178
	v_pk_mul_f32 v[30:31], v[30:31], v[184:185]
	v_cvt_pk_f32_fp8_e32 v[184:185], v181
	v_max_f32_e32 v179, v179, v179
	v_med3_f32 v161, v161, s35, v177
	v_med3_f32 v179, v179, s35, v177
	v_mul_f32_e32 v161, 0xbfb8aa3b, v161
	v_mul_f32_e32 v179, 0xbfb8aa3b, v179
	v_pk_add_f32 v[162:163], v[162:163], 1.0 op_sel_hi:[1,0]
	v_exp_f32_e32 v178, v161
	v_add_f32_e32 v161, 1.0, v188
	v_max_f32_e32 v188, v189, v189
	v_exp_f32_e32 v189, v179
	v_pk_mul_f32 v[162:163], v[186:187], v[162:163]
	v_cvt_pk_f32_fp8_e32 v[190:191], v183
	v_pk_mul_f32 v[38:39], v[38:39], v[162:163]
	v_max_f32_e32 v162, v184, v184
	v_med3_f32 v162, v162, s35, v177
	v_med3_f32 v188, v188, s35, v177
	v_mul_f32_e32 v162, 0xbfb8aa3b, v162
	v_mul_f32_e32 v179, 0xbfb8aa3b, v188
	v_rcp_f32_e32 v188, v161
	v_add_f32_e32 v161, 1.0, v189
	v_exp_f32_e32 v163, v162
	v_exp_f32_e32 v179, v179
	v_rcp_f32_e32 v189, v161
	v_max_f32_e32 v161, v190, v190
	v_med3_f32 v161, v161, s35, v177
	v_mul_f32_e32 v161, 0xbfb8aa3b, v161
	v_exp_f32_e32 v162, v161
	v_add_f32_e32 v161, 1.0, v163
	v_max_f32_e32 v163, v185, v185
	v_cvt_pk_f32_fp8_sdwa v[180:181], v181 src0_sel:WORD_1
	v_pk_add_f32 v[178:179], v[178:179], 1.0 op_sel_hi:[1,0]
	v_med3_f32 v163, v163, s35, v177
	v_pk_mul_f32 v[178:179], v[188:189], v[178:179]
	v_mul_f32_e32 v163, 0xbfb8aa3b, v163
	v_pk_mul_f32 v[40:41], v[40:41], v[178:179]
	v_exp_f32_e32 v179, v163
	v_cvt_pk_f32_fp8_sdwa v[182:183], v183 src0_sel:WORD_1
	v_rcp_f32_e32 v178, v161
	v_max_f32_e32 v161, v191, v191
	v_med3_f32 v161, v161, s35, v177
	v_max_f32_e32 v180, v180, v180
	v_mul_f32_e32 v161, 0xbfb8aa3b, v161
	v_med3_f32 v180, v180, s35, v177
	v_exp_f32_e32 v163, v161
	v_add_f32_e32 v161, 1.0, v179
	v_mul_f32_e32 v180, 0xbfb8aa3b, v180
	v_rcp_f32_e32 v179, v161
	v_max_f32_e32 v161, v182, v182
	v_exp_f32_e32 v182, v180
	v_max_f32_e32 v181, v181, v181
	v_med3_f32 v161, v161, s35, v177
	v_med3_f32 v181, v181, s35, v177
	v_mul_f32_e32 v161, 0xbfb8aa3b, v161
	v_mul_f32_e32 v181, 0xbfb8aa3b, v181
	v_exp_f32_e32 v180, v161
	v_add_f32_e32 v161, 1.0, v182
	v_max_f32_e32 v182, v183, v183
	v_exp_f32_e32 v183, v181
	v_med3_f32 v182, v182, s35, v177
	v_mul_f32_e32 v181, 0xbfb8aa3b, v182
	v_exp_f32_e32 v181, v181
	v_rcp_f32_e32 v182, v161
	v_add_f32_e32 v161, 1.0, v183
	v_pk_add_f32 v[162:163], v[162:163], 1.0 op_sel_hi:[1,0]
	v_rcp_f32_e32 v183, v161
	v_pk_mul_f32 v[162:163], v[178:179], v[162:163]
	v_pk_add_f32 v[180:181], v[180:181], 1.0 op_sel_hi:[1,0]
	v_pk_mul_f32 v[42:43], v[42:43], v[162:163]
	s_waitcnt vmcnt(27)
	v_cvt_pk_f32_fp8_e32 v[162:163], v158
	v_pk_mul_f32 v[178:179], v[182:183], v[180:181]
	s_waitcnt vmcnt(26)
	v_cvt_pk_f32_fp8_e32 v[182:183], v156
	v_pk_mul_f32 v[44:45], v[44:45], v[178:179]
	v_max_f32_e32 v162, v162, v162
	v_med3_f32 v162, v162, s35, v177
	v_mul_f32_e32 v162, 0xbfb8aa3b, v162
	v_max_f32_e32 v161, v182, v182
	v_exp_f32_e32 v182, v162
	v_med3_f32 v161, v161, s35, v177
	v_max_f32_e32 v163, v163, v163
	v_cvt_pk_f32_fp8_sdwa v[178:179], v158 src0_sel:WORD_1
	v_mul_f32_e32 v161, 0xbfb8aa3b, v161
	v_med3_f32 v163, v163, s35, v177
	v_exp_f32_e32 v162, v161
	v_add_f32_e32 v161, 1.0, v182
	v_mul_f32_e32 v163, 0xbfb8aa3b, v163
	v_rcp_f32_e32 v182, v161
	v_max_f32_e32 v161, v183, v183
	v_exp_f32_e32 v183, v163
	v_cvt_pk_f32_fp8_sdwa v[184:185], v156 src0_sel:WORD_1
	v_med3_f32 v161, v161, s35, v177
	v_max_f32_e32 v178, v178, v178
	v_mul_f32_e32 v161, 0xbfb8aa3b, v161
	v_med3_f32 v178, v178, s35, v177
	v_exp_f32_e32 v163, v161
	v_add_f32_e32 v161, 1.0, v183
	v_mul_f32_e32 v178, 0xbfb8aa3b, v178
	v_rcp_f32_e32 v183, v161
	v_max_f32_e32 v161, v184, v184
	v_exp_f32_e32 v184, v178
	v_cvt_pk_f32_fp8_e32 v[180:181], v159
	v_max_f32_e32 v179, v179, v179
	v_med3_f32 v161, v161, s35, v177
	v_med3_f32 v179, v179, s35, v177
	v_mul_f32_e32 v161, 0xbfb8aa3b, v161
	v_mul_f32_e32 v179, 0xbfb8aa3b, v179
	v_pk_add_f32 v[162:163], v[162:163], 1.0 op_sel_hi:[1,0]
	v_cvt_pk_f32_fp8_sdwa v[158:159], v159 src0_sel:WORD_1
	v_exp_f32_e32 v178, v161
	v_add_f32_e32 v161, 1.0, v184
	v_max_f32_e32 v184, v185, v185
	v_exp_f32_e32 v185, v179
	v_pk_mul_f32 v[162:163], v[182:183], v[162:163]
	v_cvt_pk_f32_fp8_e32 v[186:187], v157
	v_pk_mul_f32 v[50:51], v[50:51], v[162:163]
	v_max_f32_e32 v162, v180, v180
	v_med3_f32 v162, v162, s35, v177
	v_med3_f32 v184, v184, s35, v177
	v_mul_f32_e32 v162, 0xbfb8aa3b, v162
	v_cvt_pk_f32_fp8_sdwa v[156:157], v157 src0_sel:WORD_1
	v_mul_f32_e32 v179, 0xbfb8aa3b, v184
	v_rcp_f32_e32 v184, v161
	v_add_f32_e32 v161, 1.0, v185
	v_exp_f32_e32 v163, v162
	v_max_f32_e32 v158, v158, v158
	v_max_f32_e32 v159, v159, v159
	v_exp_f32_e32 v179, v179
	v_rcp_f32_e32 v185, v161
	v_max_f32_e32 v161, v186, v186
	v_med3_f32 v158, v158, s35, v177
	v_med3_f32 v159, v159, s35, v177
	v_med3_f32 v161, v161, s35, v177
	v_mul_f32_e32 v158, 0xbfb8aa3b, v158
	v_mul_f32_e32 v159, 0xbfb8aa3b, v159
	v_mul_f32_e32 v161, 0xbfb8aa3b, v161
	v_exp_f32_e32 v158, v158
	v_exp_f32_e32 v159, v159
	v_exp_f32_e32 v162, v161
	v_add_f32_e32 v161, 1.0, v163
	v_max_f32_e32 v163, v181, v181
	v_max_f32_e32 v156, v156, v156
	v_max_f32_e32 v157, v157, v157
	v_pk_add_f32 v[178:179], v[178:179], 1.0 op_sel_hi:[1,0]
	v_med3_f32 v163, v163, s35, v177
	v_med3_f32 v156, v156, s35, v177
	v_med3_f32 v157, v157, s35, v177
	v_pk_mul_f32 v[178:179], v[184:185], v[178:179]
	v_mul_f32_e32 v163, 0xbfb8aa3b, v163
	v_mul_f32_e32 v156, 0xbfb8aa3b, v156
	v_mul_f32_e32 v157, 0xbfb8aa3b, v157
	v_pk_mul_f32 v[52:53], v[52:53], v[178:179]
	v_exp_f32_e32 v179, v163
	v_exp_f32_e32 v156, v156
	v_add_f32_e32 v158, 1.0, v158
	v_exp_f32_e32 v157, v157
	v_add_f32_e32 v159, 1.0, v159
	v_rcp_f32_e32 v178, v161
	v_max_f32_e32 v161, v187, v187
	v_rcp_f32_e32 v158, v158
	v_rcp_f32_e32 v159, v159
	v_med3_f32 v161, v161, s35, v177
	v_mul_f32_e32 v161, 0xbfb8aa3b, v161
	v_exp_f32_e32 v163, v161
	v_add_f32_e32 v161, 1.0, v179
	v_pk_add_f32 v[156:157], v[156:157], 1.0 op_sel_hi:[1,0]
	v_rcp_f32_e32 v179, v161
	v_pk_mul_f32 v[156:157], v[158:159], v[156:157]
	v_pk_add_f32 v[162:163], v[162:163], 1.0 op_sel_hi:[1,0]
	v_pk_mul_f32 v[56:57], v[56:57], v[156:157]
	s_waitcnt vmcnt(25)
	v_cvt_pk_f32_fp8_e32 v[156:157], v154
	v_pk_mul_f32 v[162:163], v[178:179], v[162:163]
	s_waitcnt vmcnt(24)
	v_cvt_pk_f32_fp8_e32 v[178:179], v152
	v_cvt_pk_f32_fp8_sdwa v[158:159], v154 src0_sel:WORD_1
	v_max_f32_e32 v156, v156, v156
	v_med3_f32 v156, v156, s35, v177
	v_mul_f32_e32 v156, 0xbfb8aa3b, v156
	v_max_f32_e32 v161, v178, v178
	v_exp_f32_e32 v178, v156
	v_max_f32_e32 v157, v157, v157
	v_med3_f32 v157, v157, s35, v177
	v_med3_f32 v156, v161, s35, v177
	v_add_f32_e32 v161, 1.0, v178
	v_mul_f32_e32 v157, 0xbfb8aa3b, v157
	v_rcp_f32_e32 v178, v161
	v_max_f32_e32 v161, v179, v179
	v_exp_f32_e32 v179, v157
	v_cvt_pk_f32_fp8_sdwa v[180:181], v152 src0_sel:WORD_1
	v_max_f32_e32 v158, v158, v158
	v_med3_f32 v158, v158, s35, v177
	v_med3_f32 v157, v161, s35, v177
	v_add_f32_e32 v161, 1.0, v179
	v_mul_f32_e32 v158, 0xbfb8aa3b, v158
	v_rcp_f32_e32 v179, v161
	v_max_f32_e32 v161, v180, v180
	v_exp_f32_e32 v180, v158
	v_max_f32_e32 v159, v159, v159
	v_med3_f32 v159, v159, s35, v177
	v_pk_mul_f32 v[54:55], v[54:55], v[162:163]
	v_cvt_pk_f32_fp8_e32 v[162:163], v155
	v_cvt_pk_f32_fp8_sdwa v[154:155], v155 src0_sel:WORD_1
	v_mul_f32_e32 v156, 0xbfb8aa3b, v156
	v_mul_f32_e32 v157, 0xbfb8aa3b, v157
	v_mul_f32_e32 v159, 0xbfb8aa3b, v159
	v_exp_f32_e32 v156, v156
	v_exp_f32_e32 v157, v157
	v_med3_f32 v158, v161, s35, v177
	v_add_f32_e32 v161, 1.0, v180
	v_max_f32_e32 v180, v181, v181
	v_exp_f32_e32 v181, v159
	v_med3_f32 v180, v180, s35, v177
	v_cvt_pk_f32_fp8_e32 v[182:183], v153
	v_cvt_pk_f32_fp8_sdwa v[152:153], v153 src0_sel:WORD_1
	v_mul_f32_e32 v158, 0xbfb8aa3b, v158
	v_mul_f32_e32 v159, 0xbfb8aa3b, v180
	v_max_f32_e32 v154, v154, v154
	v_max_f32_e32 v155, v155, v155
	v_exp_f32_e32 v158, v158
	v_exp_f32_e32 v159, v159
	v_rcp_f32_e32 v180, v161
	v_add_f32_e32 v161, 1.0, v181
	v_pk_add_f32 v[156:157], v[156:157], 1.0 op_sel_hi:[1,0]
	v_med3_f32 v154, v154, s35, v177
	v_med3_f32 v155, v155, s35, v177
	v_rcp_f32_e32 v181, v161
	v_pk_mul_f32 v[156:157], v[178:179], v[156:157]
	v_mul_f32_e32 v154, 0xbfb8aa3b, v154
	v_mul_f32_e32 v155, 0xbfb8aa3b, v155
	v_pk_mul_f32 v[62:63], v[62:63], v[156:157]
	v_max_f32_e32 v157, v162, v162
	v_exp_f32_e32 v154, v154
	v_exp_f32_e32 v155, v155
	v_med3_f32 v157, v157, s35, v177
	v_max_f32_e32 v152, v152, v152
	v_max_f32_e32 v153, v153, v153
	v_pk_add_f32 v[158:159], v[158:159], 1.0 op_sel_hi:[1,0]
	v_mul_f32_e32 v157, 0xbfb8aa3b, v157
	v_med3_f32 v152, v152, s35, v177
	v_med3_f32 v153, v153, s35, v177
	v_pk_mul_f32 v[158:159], v[180:181], v[158:159]
	v_exp_f32_e32 v157, v157
	v_mul_f32_e32 v152, 0xbfb8aa3b, v152
	v_mul_f32_e32 v153, 0xbfb8aa3b, v153
	v_pk_mul_f32 v[64:65], v[64:65], v[158:159]
	v_max_f32_e32 v159, v163, v163
	v_exp_f32_e32 v152, v152
	v_add_f32_e32 v154, 1.0, v154
	v_exp_f32_e32 v153, v153
	v_add_f32_e32 v155, 1.0, v155
	v_med3_f32 v159, v159, s35, v177
	v_rcp_f32_e32 v154, v154
	v_rcp_f32_e32 v155, v155
	v_mul_f32_e32 v159, 0xbfb8aa3b, v159
	v_add_f32_e32 v157, 1.0, v157
	v_exp_f32_e32 v159, v159
	v_max_f32_e32 v156, v182, v182
	v_rcp_f32_e32 v158, v157
	v_max_f32_e32 v157, v183, v183
	v_pk_add_f32 v[152:153], v[152:153], 1.0 op_sel_hi:[1,0]
	v_med3_f32 v156, v156, s35, v177
	v_med3_f32 v157, v157, s35, v177
	v_pk_mul_f32 v[152:153], v[154:155], v[152:153]
	v_mul_f32_e32 v156, 0xbfb8aa3b, v156
	v_mul_f32_e32 v157, 0xbfb8aa3b, v157
	v_pk_mul_f32 v[68:69], v[68:69], v[152:153]
	s_waitcnt vmcnt(23)
	v_cvt_pk_f32_fp8_e32 v[152:153], v150
	v_exp_f32_e32 v156, v156
	v_exp_f32_e32 v157, v157
	v_add_f32_e32 v159, 1.0, v159
	v_rcp_f32_e32 v159, v159
	v_max_f32_e32 v152, v152, v152
	v_pk_add_f32 v[156:157], v[156:157], 1.0 op_sel_hi:[1,0]
	v_med3_f32 v152, v152, s35, v177
	v_pk_mul_f32 v[156:157], v[158:159], v[156:157]
	s_waitcnt vmcnt(22)
	v_cvt_pk_f32_fp8_e32 v[158:159], v148
	v_mul_f32_e32 v152, 0xbfb8aa3b, v152
	v_exp_f32_e32 v161, v152
	v_cvt_pk_f32_fp8_sdwa v[154:155], v150 src0_sel:WORD_1
	v_max_f32_e32 v153, v153, v153
	v_med3_f32 v153, v153, s35, v177
	v_max_f32_e32 v158, v158, v158
	v_mul_f32_e32 v153, 0xbfb8aa3b, v153
	v_cvt_pk_f32_fp8_sdwa v[162:163], v148 src0_sel:WORD_1
	v_med3_f32 v152, v158, s35, v177
	v_add_f32_e32 v158, 1.0, v161
	v_exp_f32_e32 v161, v153
	v_max_f32_e32 v154, v154, v154
	v_med3_f32 v154, v154, s35, v177
	v_max_f32_e32 v159, v159, v159
	v_mul_f32_e32 v154, 0xbfb8aa3b, v154
	v_med3_f32 v153, v159, s35, v177
	v_add_f32_e32 v159, 1.0, v161
	v_max_f32_e32 v161, v162, v162
	v_exp_f32_e32 v162, v154
	v_max_f32_e32 v155, v155, v155
	v_med3_f32 v155, v155, s35, v177
	v_pk_mul_f32 v[66:67], v[66:67], v[156:157]
	v_cvt_pk_f32_fp8_e32 v[156:157], v151
	v_cvt_pk_f32_fp8_sdwa v[150:151], v151 src0_sel:WORD_1
	v_mul_f32_e32 v152, 0xbfb8aa3b, v152
	v_mul_f32_e32 v153, 0xbfb8aa3b, v153
	v_mul_f32_e32 v155, 0xbfb8aa3b, v155
	v_exp_f32_e32 v152, v152
	v_exp_f32_e32 v153, v153
	v_med3_f32 v154, v161, s35, v177
	v_add_f32_e32 v161, 1.0, v162
	v_max_f32_e32 v162, v163, v163
	v_exp_f32_e32 v163, v155
	v_rcp_f32_e32 v158, v158
	v_rcp_f32_e32 v159, v159
	v_med3_f32 v162, v162, s35, v177
	v_cvt_pk_f32_fp8_e32 v[178:179], v149
	v_cvt_pk_f32_fp8_sdwa v[148:149], v149 src0_sel:WORD_1
	v_mul_f32_e32 v154, 0xbfb8aa3b, v154
	v_mul_f32_e32 v155, 0xbfb8aa3b, v162
	v_max_f32_e32 v150, v150, v150
	v_max_f32_e32 v151, v151, v151
	v_exp_f32_e32 v154, v154
	v_exp_f32_e32 v155, v155
	v_rcp_f32_e32 v162, v161
	v_add_f32_e32 v161, 1.0, v163
	v_pk_add_f32 v[152:153], v[152:153], 1.0 op_sel_hi:[1,0]
	v_med3_f32 v150, v150, s35, v177
	v_med3_f32 v151, v151, s35, v177
	v_rcp_f32_e32 v163, v161
	v_pk_mul_f32 v[152:153], v[158:159], v[152:153]
	v_mul_f32_e32 v150, 0xbfb8aa3b, v150
	v_mul_f32_e32 v151, 0xbfb8aa3b, v151
	v_pk_mul_f32 v[74:75], v[74:75], v[152:153]
	v_max_f32_e32 v153, v156, v156
	v_exp_f32_e32 v150, v150
	v_exp_f32_e32 v151, v151
	v_med3_f32 v153, v153, s35, v177
	v_max_f32_e32 v148, v148, v148
	v_max_f32_e32 v149, v149, v149
	v_pk_add_f32 v[154:155], v[154:155], 1.0 op_sel_hi:[1,0]
	v_mul_f32_e32 v153, 0xbfb8aa3b, v153
	v_med3_f32 v148, v148, s35, v177
	v_med3_f32 v149, v149, s35, v177
	v_pk_mul_f32 v[154:155], v[162:163], v[154:155]
	v_exp_f32_e32 v153, v153
	v_mul_f32_e32 v148, 0xbfb8aa3b, v148
	v_mul_f32_e32 v149, 0xbfb8aa3b, v149
	v_pk_mul_f32 v[76:77], v[76:77], v[154:155]
	v_max_f32_e32 v155, v157, v157
	v_exp_f32_e32 v148, v148
	v_add_f32_e32 v150, 1.0, v150
	v_exp_f32_e32 v149, v149
	v_add_f32_e32 v151, 1.0, v151
	v_med3_f32 v155, v155, s35, v177
	v_rcp_f32_e32 v150, v150
	v_rcp_f32_e32 v151, v151
	v_mul_f32_e32 v155, 0xbfb8aa3b, v155
	v_add_f32_e32 v153, 1.0, v153
	v_exp_f32_e32 v155, v155
	v_max_f32_e32 v152, v178, v178
	v_rcp_f32_e32 v154, v153
	v_max_f32_e32 v153, v179, v179
	v_pk_add_f32 v[148:149], v[148:149], 1.0 op_sel_hi:[1,0]
	v_med3_f32 v152, v152, s35, v177
	v_med3_f32 v153, v153, s35, v177
	v_pk_mul_f32 v[148:149], v[150:151], v[148:149]
	v_mul_f32_e32 v152, 0xbfb8aa3b, v152
	v_mul_f32_e32 v153, 0xbfb8aa3b, v153
	v_pk_mul_f32 v[80:81], v[80:81], v[148:149]
	s_waitcnt vmcnt(21)
	v_cvt_pk_f32_fp8_e32 v[148:149], v146
	v_exp_f32_e32 v152, v152
	v_exp_f32_e32 v153, v153
	v_add_f32_e32 v155, 1.0, v155
	v_rcp_f32_e32 v155, v155
	v_max_f32_e32 v148, v148, v148
	v_pk_add_f32 v[152:153], v[152:153], 1.0 op_sel_hi:[1,0]
	v_med3_f32 v148, v148, s35, v177
	v_pk_mul_f32 v[152:153], v[154:155], v[152:153]
	s_waitcnt vmcnt(20)
	v_cvt_pk_f32_fp8_e32 v[154:155], v144
	v_mul_f32_e32 v148, 0xbfb8aa3b, v148
	v_exp_f32_e32 v161, v148
	v_cvt_pk_f32_fp8_sdwa v[150:151], v146 src0_sel:WORD_1
	v_max_f32_e32 v149, v149, v149
	v_med3_f32 v149, v149, s35, v177
	v_max_f32_e32 v154, v154, v154
	v_mul_f32_e32 v149, 0xbfb8aa3b, v149
	v_med3_f32 v148, v154, s35, v177
	v_add_f32_e32 v154, 1.0, v161
	v_exp_f32_e32 v161, v149
	v_max_f32_e32 v150, v150, v150
	v_med3_f32 v150, v150, s35, v177
	v_cvt_pk_f32_fp8_sdwa v[156:157], v144 src0_sel:WORD_1
	v_max_f32_e32 v155, v155, v155
	v_mul_f32_e32 v150, 0xbfb8aa3b, v150
	v_med3_f32 v149, v155, s35, v177
	v_add_f32_e32 v155, 1.0, v161
	v_exp_f32_e32 v161, v150
	v_max_f32_e32 v151, v151, v151
	v_med3_f32 v151, v151, s35, v177
	v_pk_mul_f32 v[78:79], v[78:79], v[152:153]
	v_cvt_pk_f32_fp8_e32 v[152:153], v147
	v_cvt_pk_f32_fp8_sdwa v[146:147], v147 src0_sel:WORD_1
	v_mul_f32_e32 v148, 0xbfb8aa3b, v148
	v_mul_f32_e32 v149, 0xbfb8aa3b, v149
	v_max_f32_e32 v156, v156, v156
	v_mul_f32_e32 v151, 0xbfb8aa3b, v151
	v_exp_f32_e32 v148, v148
	v_exp_f32_e32 v149, v149
	v_med3_f32 v150, v156, s35, v177
	v_add_f32_e32 v156, 1.0, v161
	v_exp_f32_e32 v161, v151
	v_rcp_f32_e32 v154, v154
	v_rcp_f32_e32 v155, v155
	v_max_f32_e32 v157, v157, v157
	v_med3_f32 v157, v157, s35, v177
	v_cvt_pk_f32_fp8_e32 v[158:159], v145
	v_cvt_pk_f32_fp8_sdwa v[144:145], v145 src0_sel:WORD_1
	v_mul_f32_e32 v150, 0xbfb8aa3b, v150
	v_mul_f32_e32 v151, 0xbfb8aa3b, v157
	v_max_f32_e32 v146, v146, v146
	v_max_f32_e32 v147, v147, v147
	v_exp_f32_e32 v150, v150
	v_exp_f32_e32 v151, v151
	v_add_f32_e32 v157, 1.0, v161
	v_pk_add_f32 v[148:149], v[148:149], 1.0 op_sel_hi:[1,0]
	v_med3_f32 v146, v146, s35, v177
	v_med3_f32 v147, v147, s35, v177
	v_rcp_f32_e32 v156, v156
	v_rcp_f32_e32 v157, v157
	v_pk_mul_f32 v[148:149], v[154:155], v[148:149]
	v_mul_f32_e32 v146, 0xbfb8aa3b, v146
	v_mul_f32_e32 v147, 0xbfb8aa3b, v147
	v_pk_mul_f32 v[82:83], v[82:83], v[148:149]
	v_max_f32_e32 v149, v152, v152
	v_exp_f32_e32 v146, v146
	v_exp_f32_e32 v147, v147
	v_med3_f32 v149, v149, s35, v177
	v_max_f32_e32 v144, v144, v144
	v_max_f32_e32 v145, v145, v145
	v_pk_add_f32 v[150:151], v[150:151], 1.0 op_sel_hi:[1,0]
	v_mul_f32_e32 v149, 0xbfb8aa3b, v149
	v_med3_f32 v144, v144, s35, v177
	v_med3_f32 v145, v145, s35, v177
	v_pk_mul_f32 v[150:151], v[156:157], v[150:151]
	v_exp_f32_e32 v149, v149
	v_mul_f32_e32 v144, 0xbfb8aa3b, v144
	v_mul_f32_e32 v145, 0xbfb8aa3b, v145
	v_pk_mul_f32 v[84:85], v[84:85], v[150:151]
	v_max_f32_e32 v151, v153, v153
	v_exp_f32_e32 v144, v144
	v_add_f32_e32 v146, 1.0, v146
	v_exp_f32_e32 v145, v145
	v_add_f32_e32 v147, 1.0, v147
	v_med3_f32 v151, v151, s35, v177
	v_rcp_f32_e32 v146, v146
	v_rcp_f32_e32 v147, v147
	v_mul_f32_e32 v151, 0xbfb8aa3b, v151
	v_add_f32_e32 v149, 1.0, v149
	v_exp_f32_e32 v151, v151
	v_max_f32_e32 v148, v158, v158
	v_rcp_f32_e32 v150, v149
	v_max_f32_e32 v149, v159, v159
	v_pk_add_f32 v[144:145], v[144:145], 1.0 op_sel_hi:[1,0]
	v_med3_f32 v148, v148, s35, v177
	v_med3_f32 v149, v149, s35, v177
	v_pk_mul_f32 v[144:145], v[146:147], v[144:145]
	v_mul_f32_e32 v148, 0xbfb8aa3b, v148
	v_mul_f32_e32 v149, 0xbfb8aa3b, v149
	v_pk_mul_f32 v[92:93], v[92:93], v[144:145]
	s_waitcnt vmcnt(19)
	v_cvt_pk_f32_fp8_e32 v[144:145], v142
	v_exp_f32_e32 v148, v148
	v_exp_f32_e32 v149, v149
	v_add_f32_e32 v151, 1.0, v151
	v_rcp_f32_e32 v151, v151
	v_max_f32_e32 v144, v144, v144
	v_pk_add_f32 v[148:149], v[148:149], 1.0 op_sel_hi:[1,0]
	v_med3_f32 v144, v144, s35, v177
	v_pk_mul_f32 v[148:149], v[150:151], v[148:149]
	s_waitcnt vmcnt(18)
	v_cvt_pk_f32_fp8_e32 v[150:151], v140
	v_mul_f32_e32 v144, 0xbfb8aa3b, v144
	v_exp_f32_e32 v156, v144
	v_cvt_pk_f32_fp8_sdwa v[146:147], v142 src0_sel:WORD_1
	v_max_f32_e32 v145, v145, v145
	v_med3_f32 v145, v145, s35, v177
	v_max_f32_e32 v150, v150, v150
	v_mul_f32_e32 v145, 0xbfb8aa3b, v145
	v_med3_f32 v144, v150, s35, v177
	v_add_f32_e32 v150, 1.0, v156
	v_exp_f32_e32 v156, v145
	v_max_f32_e32 v146, v146, v146
	v_med3_f32 v146, v146, s35, v177
	v_cvt_pk_f32_fp8_sdwa v[152:153], v140 src0_sel:WORD_1
	v_max_f32_e32 v151, v151, v151
	v_mul_f32_e32 v146, 0xbfb8aa3b, v146
	v_med3_f32 v145, v151, s35, v177
	v_add_f32_e32 v151, 1.0, v156
	v_exp_f32_e32 v156, v146
	v_max_f32_e32 v147, v147, v147
	v_med3_f32 v147, v147, s35, v177
	v_pk_mul_f32 v[90:91], v[90:91], v[148:149]
	v_cvt_pk_f32_fp8_e32 v[148:149], v143
	v_cvt_pk_f32_fp8_sdwa v[142:143], v143 src0_sel:WORD_1
	v_mul_f32_e32 v144, 0xbfb8aa3b, v144
	v_mul_f32_e32 v145, 0xbfb8aa3b, v145
	v_max_f32_e32 v152, v152, v152
	v_mul_f32_e32 v147, 0xbfb8aa3b, v147
	v_exp_f32_e32 v144, v144
	v_exp_f32_e32 v145, v145
	v_med3_f32 v146, v152, s35, v177
	v_add_f32_e32 v152, 1.0, v156
	v_exp_f32_e32 v156, v147
	v_rcp_f32_e32 v150, v150
	v_rcp_f32_e32 v151, v151
	v_max_f32_e32 v153, v153, v153
	v_med3_f32 v153, v153, s35, v177
	v_cvt_pk_f32_fp8_e32 v[154:155], v141
	v_cvt_pk_f32_fp8_sdwa v[140:141], v141 src0_sel:WORD_1
	v_mul_f32_e32 v146, 0xbfb8aa3b, v146
	v_mul_f32_e32 v147, 0xbfb8aa3b, v153
	v_max_f32_e32 v142, v142, v142
	v_max_f32_e32 v143, v143, v143
	v_exp_f32_e32 v146, v146
	v_exp_f32_e32 v147, v147
	v_add_f32_e32 v153, 1.0, v156
	v_pk_add_f32 v[144:145], v[144:145], 1.0 op_sel_hi:[1,0]
	v_med3_f32 v142, v142, s35, v177
	v_med3_f32 v143, v143, s35, v177
	v_rcp_f32_e32 v152, v152
	v_rcp_f32_e32 v153, v153
	v_pk_mul_f32 v[144:145], v[150:151], v[144:145]
	v_mul_f32_e32 v142, 0xbfb8aa3b, v142
	v_mul_f32_e32 v143, 0xbfb8aa3b, v143
	v_pk_mul_f32 v[94:95], v[94:95], v[144:145]
	v_max_f32_e32 v145, v148, v148
	v_exp_f32_e32 v142, v142
	v_exp_f32_e32 v143, v143
	v_med3_f32 v145, v145, s35, v177
	v_max_f32_e32 v140, v140, v140
	v_max_f32_e32 v141, v141, v141
	v_pk_add_f32 v[146:147], v[146:147], 1.0 op_sel_hi:[1,0]
	v_mul_f32_e32 v145, 0xbfb8aa3b, v145
	v_med3_f32 v140, v140, s35, v177
	v_med3_f32 v141, v141, s35, v177
	v_pk_mul_f32 v[146:147], v[152:153], v[146:147]
	v_exp_f32_e32 v145, v145
	v_mul_f32_e32 v140, 0xbfb8aa3b, v140
	v_mul_f32_e32 v141, 0xbfb8aa3b, v141
	v_pk_mul_f32 v[96:97], v[96:97], v[146:147]
	v_max_f32_e32 v147, v149, v149
	v_exp_f32_e32 v140, v140
	v_add_f32_e32 v142, 1.0, v142
	v_exp_f32_e32 v141, v141
	v_add_f32_e32 v143, 1.0, v143
	v_med3_f32 v147, v147, s35, v177
	v_rcp_f32_e32 v142, v142
	v_rcp_f32_e32 v143, v143
	v_mul_f32_e32 v147, 0xbfb8aa3b, v147
	v_add_f32_e32 v145, 1.0, v145
	v_exp_f32_e32 v147, v147
	v_max_f32_e32 v144, v154, v154
	v_rcp_f32_e32 v146, v145
	v_max_f32_e32 v145, v155, v155
	v_pk_add_f32 v[140:141], v[140:141], 1.0 op_sel_hi:[1,0]
	v_med3_f32 v144, v144, s35, v177
	v_med3_f32 v145, v145, s35, v177
	v_pk_mul_f32 v[140:141], v[142:143], v[140:141]
	v_mul_f32_e32 v144, 0xbfb8aa3b, v144
	v_mul_f32_e32 v145, 0xbfb8aa3b, v145
	v_pk_mul_f32 v[104:105], v[104:105], v[140:141]
	s_waitcnt vmcnt(17)
	v_cvt_pk_f32_fp8_e32 v[140:141], v138
	v_exp_f32_e32 v144, v144
	v_exp_f32_e32 v145, v145
	v_add_f32_e32 v147, 1.0, v147
	v_rcp_f32_e32 v147, v147
	v_max_f32_e32 v140, v140, v140
	v_pk_add_f32 v[144:145], v[144:145], 1.0 op_sel_hi:[1,0]
	v_med3_f32 v140, v140, s35, v177
	v_pk_mul_f32 v[144:145], v[146:147], v[144:145]
	s_waitcnt vmcnt(16)
	v_cvt_pk_f32_fp8_e32 v[146:147], v136
	v_mul_f32_e32 v140, 0xbfb8aa3b, v140
	v_exp_f32_e32 v152, v140
	v_cvt_pk_f32_fp8_sdwa v[142:143], v138 src0_sel:WORD_1
	v_max_f32_e32 v141, v141, v141
	v_med3_f32 v141, v141, s35, v177
	v_max_f32_e32 v146, v146, v146
	v_mul_f32_e32 v141, 0xbfb8aa3b, v141
	v_med3_f32 v140, v146, s35, v177
	v_add_f32_e32 v146, 1.0, v152
	v_exp_f32_e32 v152, v141
	v_max_f32_e32 v142, v142, v142
	v_med3_f32 v142, v142, s35, v177
	v_cvt_pk_f32_fp8_sdwa v[148:149], v136 src0_sel:WORD_1
	v_max_f32_e32 v147, v147, v147
	v_mul_f32_e32 v142, 0xbfb8aa3b, v142
	v_med3_f32 v141, v147, s35, v177
	v_add_f32_e32 v147, 1.0, v152
	v_exp_f32_e32 v152, v142
	v_max_f32_e32 v143, v143, v143
	v_med3_f32 v143, v143, s35, v177
	v_mul_f32_e32 v140, 0xbfb8aa3b, v140
	v_mul_f32_e32 v141, 0xbfb8aa3b, v141
	v_max_f32_e32 v148, v148, v148
	v_mul_f32_e32 v143, 0xbfb8aa3b, v143
	v_exp_f32_e32 v140, v140
	v_exp_f32_e32 v141, v141
	v_med3_f32 v142, v148, s35, v177
	v_add_f32_e32 v148, 1.0, v152
	v_exp_f32_e32 v152, v143
	v_rcp_f32_e32 v146, v146
	v_rcp_f32_e32 v147, v147
	v_max_f32_e32 v149, v149, v149
	v_pk_mul_f32 v[102:103], v[102:103], v[144:145]
	v_cvt_pk_f32_fp8_e32 v[144:145], v139
	v_med3_f32 v149, v149, s35, v177
	v_mul_f32_e32 v142, 0xbfb8aa3b, v142
	v_mul_f32_e32 v143, 0xbfb8aa3b, v149
	v_exp_f32_e32 v142, v142
	v_exp_f32_e32 v143, v143
	v_add_f32_e32 v149, 1.0, v152
	v_pk_add_f32 v[140:141], v[140:141], 1.0 op_sel_hi:[1,0]
	v_rcp_f32_e32 v148, v148
	v_rcp_f32_e32 v149, v149
	v_pk_mul_f32 v[140:141], v[146:147], v[140:141]
	v_cvt_pk_f32_fp8_sdwa v[138:139], v139 src0_sel:WORD_1
	v_pk_mul_f32 v[106:107], v[106:107], v[140:141]
	v_max_f32_e32 v141, v144, v144
	v_med3_f32 v141, v141, s35, v177
	v_pk_add_f32 v[142:143], v[142:143], 1.0 op_sel_hi:[1,0]
	v_mul_f32_e32 v141, 0xbfb8aa3b, v141
	v_pk_mul_f32 v[142:143], v[148:149], v[142:143]
	v_exp_f32_e32 v141, v141
	v_cvt_pk_f32_fp8_e32 v[150:151], v137
	v_cvt_pk_f32_fp8_sdwa v[136:137], v137 src0_sel:WORD_1
	v_pk_mul_f32 v[108:109], v[108:109], v[142:143]
	v_max_f32_e32 v143, v145, v145
	v_max_f32_e32 v138, v138, v138
	v_max_f32_e32 v139, v139, v139
	v_med3_f32 v143, v143, s35, v177
	v_med3_f32 v138, v138, s35, v177
	v_med3_f32 v139, v139, s35, v177
	v_mul_f32_e32 v143, 0xbfb8aa3b, v143
	v_mul_f32_e32 v138, 0xbfb8aa3b, v138
	v_mul_f32_e32 v139, 0xbfb8aa3b, v139
	v_add_f32_e32 v141, 1.0, v141
	v_exp_f32_e32 v143, v143
	v_exp_f32_e32 v138, v138
	v_exp_f32_e32 v139, v139
	v_max_f32_e32 v140, v150, v150
	v_rcp_f32_e32 v142, v141
	v_max_f32_e32 v141, v151, v151
	v_max_f32_e32 v136, v136, v136
	v_max_f32_e32 v137, v137, v137
	v_med3_f32 v140, v140, s35, v177
	v_med3_f32 v141, v141, s35, v177
	v_med3_f32 v136, v136, s35, v177
	v_med3_f32 v137, v137, s35, v177
	v_mul_f32_e32 v140, 0xbfb8aa3b, v140
	v_mul_f32_e32 v141, 0xbfb8aa3b, v141
	v_mul_f32_e32 v136, 0xbfb8aa3b, v136
	v_mul_f32_e32 v137, 0xbfb8aa3b, v137
	v_exp_f32_e32 v140, v140
	v_exp_f32_e32 v141, v141
	v_add_f32_e32 v143, 1.0, v143
	v_exp_f32_e32 v136, v136
	v_add_f32_e32 v138, 1.0, v138
	v_exp_f32_e32 v137, v137
	v_add_f32_e32 v139, 1.0, v139
	v_rcp_f32_e32 v143, v143
	v_rcp_f32_e32 v138, v138
	v_rcp_f32_e32 v139, v139
	v_pk_add_f32 v[136:137], v[136:137], 1.0 op_sel_hi:[1,0]
	v_pk_add_f32 v[140:141], v[140:141], 1.0 op_sel_hi:[1,0]
	v_pk_mul_f32 v[136:137], v[138:139], v[136:137]
	v_pk_mul_f32 v[140:141], v[142:143], v[140:141]
	v_pk_mul_f32 v[116:117], v[116:117], v[136:137]
	v_pk_mul_f32 v[114:115], v[114:115], v[140:141]
	s_nop 0
	s_waitcnt vmcnt(0)
	v_mov_b64_e32 v[162:163], v[220:221]
	v_mov_b64_e32 v[160:161], v[222:223]
	v_mov_b64_e32 v[178:179], v[224:225]
	v_mov_b64_e32 v[180:181], v[226:227]
	v_mov_b64_e32 v[158:159], v[228:229]
	v_mov_b64_e32 v[156:157], v[230:231]
	v_mov_b64_e32 v[154:155], v[232:233]
	v_mov_b64_e32 v[152:153], v[234:235]
	v_mov_b64_e32 v[150:151], v[236:237]
	v_mov_b64_e32 v[148:149], v[238:239]
	v_mov_b64_e32 v[146:147], v[240:241]
	v_mov_b64_e32 v[144:145], v[242:243]
	v_mov_b64_e32 v[142:143], v[244:245]
	v_mov_b64_e32 v[140:141], v[246:247]
	v_mov_b64_e32 v[138:139], v[248:249]
	v_mov_b64_e32 v[136:137], v[250:251]
	s_waitcnt vmcnt(15)
	v_cvt_pk_f32_fp8_e32 v[182:183], v162
	s_waitcnt vmcnt(14)
	v_cvt_pk_f32_fp8_e32 v[188:189], v160
	v_cvt_pk_f32_fp8_sdwa v[184:185], v162 src0_sel:WORD_1
	v_cvt_pk_f32_fp8_sdwa v[190:191], v160 src0_sel:WORD_1
	v_max_f32_e32 v182, v182, v182
	v_med3_f32 v182, v182, s35, v177
	v_mul_f32_e32 v182, 0xbfb8aa3b, v182
	v_max_f32_e32 v134, v188, v188
	v_exp_f32_e32 v188, v182
	v_med3_f32 v134, v134, s35, v177
	v_max_f32_e32 v183, v183, v183
	v_mul_f32_e32 v134, 0xbfb8aa3b, v134
	v_med3_f32 v183, v183, s35, v177
	v_exp_f32_e32 v182, v134
	v_add_f32_e32 v134, 1.0, v188
	v_mul_f32_e32 v183, 0xbfb8aa3b, v183
	v_rcp_f32_e32 v188, v134
	v_max_f32_e32 v134, v189, v189
	v_exp_f32_e32 v189, v183
	v_med3_f32 v134, v134, s35, v177
	v_max_f32_e32 v184, v184, v184
	v_mul_f32_e32 v134, 0xbfb8aa3b, v134
	v_med3_f32 v184, v184, s35, v177
	v_exp_f32_e32 v183, v134
	v_add_f32_e32 v134, 1.0, v189
	v_mul_f32_e32 v184, 0xbfb8aa3b, v184
	v_rcp_f32_e32 v189, v134
	v_max_f32_e32 v134, v190, v190
	v_exp_f32_e32 v190, v184
	v_cvt_pk_f32_fp8_e32 v[186:187], v163
	v_max_f32_e32 v185, v185, v185
	v_med3_f32 v134, v134, s35, v177
	v_med3_f32 v185, v185, s35, v177
	v_mul_f32_e32 v134, 0xbfb8aa3b, v134
	v_mul_f32_e32 v185, 0xbfb8aa3b, v185
	v_pk_add_f32 v[182:183], v[182:183], 1.0 op_sel_hi:[1,0]
	v_exp_f32_e32 v184, v134
	v_add_f32_e32 v134, 1.0, v190
	v_max_f32_e32 v190, v191, v191
	v_exp_f32_e32 v191, v185
	v_pk_mul_f32 v[182:183], v[188:189], v[182:183]
	v_cvt_pk_f32_fp8_e32 v[192:193], v161
	v_pk_mul_f32 v[118:119], v[118:119], v[182:183]
	v_max_f32_e32 v182, v186, v186
	v_med3_f32 v182, v182, s35, v177
	v_med3_f32 v190, v190, s35, v177
	v_mul_f32_e32 v182, 0xbfb8aa3b, v182
	v_mul_f32_e32 v185, 0xbfb8aa3b, v190
	v_rcp_f32_e32 v190, v134
	v_add_f32_e32 v134, 1.0, v191
	v_exp_f32_e32 v183, v182
	v_exp_f32_e32 v185, v185
	v_rcp_f32_e32 v191, v134
	v_max_f32_e32 v134, v192, v192
	v_med3_f32 v134, v134, s35, v177
	v_mul_f32_e32 v134, 0xbfb8aa3b, v134
	v_exp_f32_e32 v182, v134
	v_add_f32_e32 v134, 1.0, v183
	v_max_f32_e32 v183, v187, v187
	v_pk_add_f32 v[184:185], v[184:185], 1.0 op_sel_hi:[1,0]
	v_med3_f32 v183, v183, s35, v177
	v_pk_mul_f32 v[184:185], v[190:191], v[184:185]
	v_mul_f32_e32 v183, 0xbfb8aa3b, v183
	v_pk_mul_f32 v[120:121], v[120:121], v[184:185]
	v_exp_f32_e32 v185, v183
	v_cvt_pk_f32_fp8_sdwa v[162:163], v163 src0_sel:WORD_1
	v_cvt_pk_f32_fp8_sdwa v[160:161], v161 src0_sel:WORD_1
	v_rcp_f32_e32 v184, v134
	v_max_f32_e32 v134, v193, v193
	v_med3_f32 v134, v134, s35, v177
	v_mul_f32_e32 v134, 0xbfb8aa3b, v134
	v_exp_f32_e32 v183, v134
	v_add_f32_e32 v134, 1.0, v185
	v_rcp_f32_e32 v185, v134
	v_max_f32_e32 v134, v160, v160
	v_max_f32_e32 v160, v162, v162
	v_med3_f32 v160, v160, s35, v177
	v_mul_f32_e32 v160, 0xbfb8aa3b, v160
	v_exp_f32_e32 v162, v160
	v_med3_f32 v134, v134, s35, v177
	v_mul_f32_e32 v134, 0xbfb8aa3b, v134
	v_exp_f32_e32 v160, v134
	v_add_f32_e32 v134, 1.0, v162
	v_max_f32_e32 v162, v163, v163
	v_med3_f32 v162, v162, s35, v177
	v_mul_f32_e32 v162, 0xbfb8aa3b, v162
	v_exp_f32_e32 v163, v162
	v_max_f32_e32 v161, v161, v161
	v_med3_f32 v161, v161, s35, v177
	v_mul_f32_e32 v161, 0xbfb8aa3b, v161
	v_exp_f32_e32 v161, v161
	v_rcp_f32_e32 v162, v134
	v_add_f32_e32 v134, 1.0, v163
	v_rcp_f32_e32 v163, v134
	v_pk_add_f32 v[160:161], v[160:161], 1.0 op_sel_hi:[1,0]
	v_pk_add_f32 v[182:183], v[182:183], 1.0 op_sel_hi:[1,0]
	s_waitcnt vmcnt(12)
	v_cvt_pk_f32_fp8_sdwa v[186:187], v180 src0_sel:WORD_1
	v_pk_mul_f32 v[160:161], v[162:163], v[160:161]
	v_pk_mul_f32 v[182:183], v[184:185], v[182:183]
	v_pk_mul_f32 v[128:129], v[128:129], v[160:161]
	v_cvt_pk_f32_fp8_e32 v[160:161], v178
	v_cvt_pk_f32_fp8_e32 v[184:185], v180
	v_cvt_pk_f32_fp8_sdwa v[162:163], v178 src0_sel:WORD_1
	v_pk_mul_f32 v[126:127], v[126:127], v[182:183]
	v_max_f32_e32 v160, v160, v160
	v_med3_f32 v160, v160, s35, v177
	v_mul_f32_e32 v160, 0xbfb8aa3b, v160
	v_max_f32_e32 v134, v184, v184
	v_exp_f32_e32 v184, v160
	v_med3_f32 v134, v134, s35, v177
	v_max_f32_e32 v161, v161, v161
	v_mul_f32_e32 v134, 0xbfb8aa3b, v134
	v_med3_f32 v161, v161, s35, v177
	v_exp_f32_e32 v160, v134
	v_add_f32_e32 v134, 1.0, v184
	v_mul_f32_e32 v161, 0xbfb8aa3b, v161
	v_rcp_f32_e32 v184, v134
	v_max_f32_e32 v134, v185, v185
	v_exp_f32_e32 v185, v161
	v_med3_f32 v134, v134, s35, v177
	v_max_f32_e32 v162, v162, v162
	v_mul_f32_e32 v134, 0xbfb8aa3b, v134
	v_med3_f32 v162, v162, s35, v177
	v_exp_f32_e32 v161, v134
	v_add_f32_e32 v134, 1.0, v185
	v_mul_f32_e32 v162, 0xbfb8aa3b, v162
	v_rcp_f32_e32 v185, v134
	v_max_f32_e32 v134, v186, v186
	v_exp_f32_e32 v186, v162
	v_cvt_pk_f32_fp8_e32 v[182:183], v179
	v_max_f32_e32 v163, v163, v163
	v_med3_f32 v134, v134, s35, v177
	v_med3_f32 v163, v163, s35, v177
	v_mul_f32_e32 v134, 0xbfb8aa3b, v134
	v_mul_f32_e32 v163, 0xbfb8aa3b, v163
	v_pk_add_f32 v[160:161], v[160:161], 1.0 op_sel_hi:[1,0]
	v_exp_f32_e32 v162, v134
	v_add_f32_e32 v134, 1.0, v186
	v_max_f32_e32 v186, v187, v187
	v_exp_f32_e32 v187, v163
	v_pk_mul_f32 v[160:161], v[184:185], v[160:161]
	v_cvt_pk_f32_fp8_e32 v[188:189], v181
	v_pk_mul_f32 v[122:123], v[122:123], v[160:161]
	v_max_f32_e32 v160, v182, v182
	v_med3_f32 v160, v160, s35, v177
	v_med3_f32 v186, v186, s35, v177
	v_mul_f32_e32 v160, 0xbfb8aa3b, v160
	v_mul_f32_e32 v163, 0xbfb8aa3b, v186
	v_rcp_f32_e32 v186, v134
	v_add_f32_e32 v134, 1.0, v187
	v_exp_f32_e32 v161, v160
	v_exp_f32_e32 v163, v163
	v_rcp_f32_e32 v187, v134
	v_max_f32_e32 v134, v188, v188
	v_med3_f32 v134, v134, s35, v177
	v_mul_f32_e32 v134, 0xbfb8aa3b, v134
	v_exp_f32_e32 v160, v134
	v_add_f32_e32 v134, 1.0, v161
	v_max_f32_e32 v161, v183, v183
	v_cvt_pk_f32_fp8_sdwa v[178:179], v179 src0_sel:WORD_1
	v_pk_add_f32 v[162:163], v[162:163], 1.0 op_sel_hi:[1,0]
	v_med3_f32 v161, v161, s35, v177
	v_pk_mul_f32 v[162:163], v[186:187], v[162:163]
	v_mul_f32_e32 v161, 0xbfb8aa3b, v161
	v_pk_mul_f32 v[124:125], v[124:125], v[162:163]
	v_exp_f32_e32 v163, v161
	v_cvt_pk_f32_fp8_sdwa v[180:181], v181 src0_sel:WORD_1
	v_rcp_f32_e32 v162, v134
	v_max_f32_e32 v134, v189, v189
	v_med3_f32 v134, v134, s35, v177
	v_max_f32_e32 v178, v178, v178
	v_mul_f32_e32 v134, 0xbfb8aa3b, v134
	v_med3_f32 v178, v178, s35, v177
	v_exp_f32_e32 v161, v134
	v_add_f32_e32 v134, 1.0, v163
	v_mul_f32_e32 v178, 0xbfb8aa3b, v178
	v_rcp_f32_e32 v163, v134
	v_max_f32_e32 v134, v180, v180
	v_exp_f32_e32 v180, v178
	v_max_f32_e32 v179, v179, v179
	v_med3_f32 v134, v134, s35, v177
	v_med3_f32 v179, v179, s35, v177
	v_mul_f32_e32 v134, 0xbfb8aa3b, v134
	v_mul_f32_e32 v179, 0xbfb8aa3b, v179
	v_exp_f32_e32 v178, v134
	v_add_f32_e32 v134, 1.0, v180
	v_max_f32_e32 v180, v181, v181
	v_exp_f32_e32 v181, v179
	v_med3_f32 v180, v180, s35, v177
	v_mul_f32_e32 v179, 0xbfb8aa3b, v180
	v_exp_f32_e32 v179, v179
	v_rcp_f32_e32 v180, v134
	v_add_f32_e32 v134, 1.0, v181
	v_pk_add_f32 v[160:161], v[160:161], 1.0 op_sel_hi:[1,0]
	v_rcp_f32_e32 v181, v134
	v_pk_mul_f32 v[160:161], v[162:163], v[160:161]
	v_pk_add_f32 v[178:179], v[178:179], 1.0 op_sel_hi:[1,0]
	v_pk_mul_f32 v[110:111], v[110:111], v[160:161]
	s_waitcnt vmcnt(11)
	v_cvt_pk_f32_fp8_e32 v[160:161], v158
	v_pk_mul_f32 v[162:163], v[180:181], v[178:179]
	s_waitcnt vmcnt(10)
	v_cvt_pk_f32_fp8_e32 v[180:181], v156
	v_pk_mul_f32 v[112:113], v[112:113], v[162:163]
	v_max_f32_e32 v160, v160, v160
	v_med3_f32 v160, v160, s35, v177
	v_mul_f32_e32 v160, 0xbfb8aa3b, v160
	v_max_f32_e32 v134, v180, v180
	v_exp_f32_e32 v180, v160
	v_med3_f32 v134, v134, s35, v177
	v_max_f32_e32 v161, v161, v161
	v_cvt_pk_f32_fp8_sdwa v[162:163], v158 src0_sel:WORD_1
	v_mul_f32_e32 v134, 0xbfb8aa3b, v134
	v_med3_f32 v161, v161, s35, v177
	v_exp_f32_e32 v160, v134
	v_add_f32_e32 v134, 1.0, v180
	v_mul_f32_e32 v161, 0xbfb8aa3b, v161
	v_rcp_f32_e32 v180, v134
	v_max_f32_e32 v134, v181, v181
	v_exp_f32_e32 v181, v161
	v_cvt_pk_f32_fp8_sdwa v[182:183], v156 src0_sel:WORD_1
	v_med3_f32 v134, v134, s35, v177
	v_max_f32_e32 v162, v162, v162
	v_mul_f32_e32 v134, 0xbfb8aa3b, v134
	v_med3_f32 v162, v162, s35, v177
	v_exp_f32_e32 v161, v134
	v_add_f32_e32 v134, 1.0, v181
	v_mul_f32_e32 v162, 0xbfb8aa3b, v162
	v_rcp_f32_e32 v181, v134
	v_max_f32_e32 v134, v182, v182
	v_exp_f32_e32 v182, v162
	v_cvt_pk_f32_fp8_e32 v[178:179], v159
	v_max_f32_e32 v163, v163, v163
	v_med3_f32 v134, v134, s35, v177
	v_med3_f32 v163, v163, s35, v177
	v_mul_f32_e32 v134, 0xbfb8aa3b, v134
	v_mul_f32_e32 v163, 0xbfb8aa3b, v163
	v_pk_add_f32 v[160:161], v[160:161], 1.0 op_sel_hi:[1,0]
	v_exp_f32_e32 v162, v134
	v_add_f32_e32 v134, 1.0, v182
	v_max_f32_e32 v182, v183, v183
	v_exp_f32_e32 v183, v163
	v_pk_mul_f32 v[160:161], v[180:181], v[160:161]
	v_cvt_pk_f32_fp8_e32 v[184:185], v157
	v_pk_mul_f32 v[98:99], v[98:99], v[160:161]
	v_max_f32_e32 v160, v178, v178
	v_med3_f32 v160, v160, s35, v177
	v_med3_f32 v182, v182, s35, v177
	v_mul_f32_e32 v160, 0xbfb8aa3b, v160
	v_mul_f32_e32 v163, 0xbfb8aa3b, v182
	v_rcp_f32_e32 v182, v134
	v_add_f32_e32 v134, 1.0, v183
	v_exp_f32_e32 v161, v160
	v_exp_f32_e32 v163, v163
	v_rcp_f32_e32 v183, v134
	v_max_f32_e32 v134, v184, v184
	v_med3_f32 v134, v134, s35, v177
	v_mul_f32_e32 v134, 0xbfb8aa3b, v134
	v_exp_f32_e32 v160, v134
	v_add_f32_e32 v134, 1.0, v161
	v_max_f32_e32 v161, v179, v179
	v_pk_add_f32 v[162:163], v[162:163], 1.0 op_sel_hi:[1,0]
	v_med3_f32 v161, v161, s35, v177
	v_pk_mul_f32 v[162:163], v[182:183], v[162:163]
	v_mul_f32_e32 v161, 0xbfb8aa3b, v161
	v_pk_mul_f32 v[100:101], v[100:101], v[162:163]
	v_exp_f32_e32 v163, v161
	v_cvt_pk_f32_fp8_sdwa v[158:159], v159 src0_sel:WORD_1
	v_cvt_pk_f32_fp8_sdwa v[156:157], v157 src0_sel:WORD_1
	v_rcp_f32_e32 v162, v134
	v_max_f32_e32 v134, v185, v185
	v_med3_f32 v134, v134, s35, v177
	v_mul_f32_e32 v134, 0xbfb8aa3b, v134
	v_exp_f32_e32 v161, v134
	v_add_f32_e32 v134, 1.0, v163
	v_rcp_f32_e32 v163, v134
	v_max_f32_e32 v134, v156, v156
	v_max_f32_e32 v156, v158, v158
	v_med3_f32 v156, v156, s35, v177
	v_mul_f32_e32 v156, 0xbfb8aa3b, v156
	v_exp_f32_e32 v158, v156
	v_med3_f32 v134, v134, s35, v177
	v_mul_f32_e32 v134, 0xbfb8aa3b, v134
	v_exp_f32_e32 v156, v134
	v_add_f32_e32 v134, 1.0, v158
	v_max_f32_e32 v158, v159, v159
	v_med3_f32 v158, v158, s35, v177
	v_mul_f32_e32 v158, 0xbfb8aa3b, v158
	v_exp_f32_e32 v159, v158
	v_max_f32_e32 v157, v157, v157
	v_med3_f32 v157, v157, s35, v177
	v_mul_f32_e32 v157, 0xbfb8aa3b, v157
	v_exp_f32_e32 v157, v157
	v_rcp_f32_e32 v158, v134
	v_add_f32_e32 v134, 1.0, v159
	v_rcp_f32_e32 v159, v134
	v_pk_add_f32 v[156:157], v[156:157], 1.0 op_sel_hi:[1,0]
	v_pk_add_f32 v[160:161], v[160:161], 1.0 op_sel_hi:[1,0]
	s_waitcnt vmcnt(8)
	v_cvt_pk_f32_fp8_sdwa v[178:179], v152 src0_sel:WORD_1
	v_pk_mul_f32 v[156:157], v[158:159], v[156:157]
	v_pk_mul_f32 v[160:161], v[162:163], v[160:161]
	v_pk_mul_f32 v[88:89], v[88:89], v[156:157]
	v_cvt_pk_f32_fp8_e32 v[156:157], v154
	v_cvt_pk_f32_fp8_e32 v[162:163], v152
	v_cvt_pk_f32_fp8_sdwa v[158:159], v154 src0_sel:WORD_1
	v_pk_mul_f32 v[86:87], v[86:87], v[160:161]
	v_max_f32_e32 v156, v156, v156
	v_med3_f32 v156, v156, s35, v177
	v_mul_f32_e32 v156, 0xbfb8aa3b, v156
	v_max_f32_e32 v134, v162, v162
	v_exp_f32_e32 v162, v156
	v_med3_f32 v134, v134, s35, v177
	v_max_f32_e32 v157, v157, v157
	v_mul_f32_e32 v134, 0xbfb8aa3b, v134
	v_med3_f32 v157, v157, s35, v177
	v_exp_f32_e32 v156, v134
	v_add_f32_e32 v134, 1.0, v162
	v_mul_f32_e32 v157, 0xbfb8aa3b, v157
	v_rcp_f32_e32 v162, v134
	v_max_f32_e32 v134, v163, v163
	v_exp_f32_e32 v163, v157
	v_med3_f32 v134, v134, s35, v177
	v_max_f32_e32 v158, v158, v158
	v_mul_f32_e32 v134, 0xbfb8aa3b, v134
	v_med3_f32 v158, v158, s35, v177
	v_exp_f32_e32 v157, v134
	v_add_f32_e32 v134, 1.0, v163
	v_mul_f32_e32 v158, 0xbfb8aa3b, v158
	v_rcp_f32_e32 v163, v134
	v_max_f32_e32 v134, v178, v178
	v_exp_f32_e32 v178, v158
	v_cvt_pk_f32_fp8_e32 v[160:161], v155
	v_max_f32_e32 v159, v159, v159
	v_med3_f32 v134, v134, s35, v177
	v_med3_f32 v159, v159, s35, v177
	v_mul_f32_e32 v134, 0xbfb8aa3b, v134
	v_mul_f32_e32 v159, 0xbfb8aa3b, v159
	v_pk_add_f32 v[156:157], v[156:157], 1.0 op_sel_hi:[1,0]
	v_exp_f32_e32 v158, v134
	v_add_f32_e32 v134, 1.0, v178
	v_max_f32_e32 v178, v179, v179
	v_exp_f32_e32 v179, v159
	v_pk_mul_f32 v[156:157], v[162:163], v[156:157]
	v_cvt_pk_f32_fp8_e32 v[180:181], v153
	v_pk_mul_f32 v[70:71], v[70:71], v[156:157]
	v_max_f32_e32 v156, v160, v160
	v_med3_f32 v156, v156, s35, v177
	v_med3_f32 v178, v178, s35, v177
	v_mul_f32_e32 v156, 0xbfb8aa3b, v156
	v_mul_f32_e32 v159, 0xbfb8aa3b, v178
	v_rcp_f32_e32 v178, v134
	v_add_f32_e32 v134, 1.0, v179
	v_exp_f32_e32 v157, v156
	v_exp_f32_e32 v159, v159
	v_rcp_f32_e32 v179, v134
	v_max_f32_e32 v134, v180, v180
	v_med3_f32 v134, v134, s35, v177
	v_mul_f32_e32 v134, 0xbfb8aa3b, v134
	v_exp_f32_e32 v156, v134
	v_add_f32_e32 v134, 1.0, v157
	v_max_f32_e32 v157, v161, v161
	v_pk_add_f32 v[158:159], v[158:159], 1.0 op_sel_hi:[1,0]
	v_med3_f32 v157, v157, s35, v177
	v_pk_mul_f32 v[158:159], v[178:179], v[158:159]
	v_mul_f32_e32 v157, 0xbfb8aa3b, v157
	v_pk_mul_f32 v[72:73], v[72:73], v[158:159]
	v_exp_f32_e32 v159, v157
	v_cvt_pk_f32_fp8_sdwa v[154:155], v155 src0_sel:WORD_1
	v_cvt_pk_f32_fp8_sdwa v[152:153], v153 src0_sel:WORD_1
	v_rcp_f32_e32 v158, v134
	v_max_f32_e32 v134, v181, v181
	v_med3_f32 v134, v134, s35, v177
	v_mul_f32_e32 v134, 0xbfb8aa3b, v134
	v_exp_f32_e32 v157, v134
	v_add_f32_e32 v134, 1.0, v159
	v_rcp_f32_e32 v159, v134
	v_max_f32_e32 v134, v152, v152
	v_max_f32_e32 v152, v154, v154
	v_med3_f32 v152, v152, s35, v177
	v_mul_f32_e32 v152, 0xbfb8aa3b, v152
	v_exp_f32_e32 v154, v152
	v_med3_f32 v134, v134, s35, v177
	v_mul_f32_e32 v134, 0xbfb8aa3b, v134
	v_exp_f32_e32 v152, v134
	v_add_f32_e32 v134, 1.0, v154
	v_max_f32_e32 v154, v155, v155
	v_med3_f32 v154, v154, s35, v177
	v_mul_f32_e32 v154, 0xbfb8aa3b, v154
	v_exp_f32_e32 v155, v154
	v_max_f32_e32 v153, v153, v153
	v_med3_f32 v153, v153, s35, v177
	v_mul_f32_e32 v153, 0xbfb8aa3b, v153
	v_exp_f32_e32 v153, v153
	v_rcp_f32_e32 v154, v134
	v_add_f32_e32 v134, 1.0, v155
	v_rcp_f32_e32 v155, v134
	v_pk_add_f32 v[152:153], v[152:153], 1.0 op_sel_hi:[1,0]
	v_pk_add_f32 v[156:157], v[156:157], 1.0 op_sel_hi:[1,0]
	s_waitcnt vmcnt(6)
	v_cvt_pk_f32_fp8_sdwa v[160:161], v148 src0_sel:WORD_1
	v_pk_mul_f32 v[152:153], v[154:155], v[152:153]
	v_pk_mul_f32 v[156:157], v[158:159], v[156:157]
	v_pk_mul_f32 v[60:61], v[60:61], v[152:153]
	v_cvt_pk_f32_fp8_e32 v[152:153], v150
	v_cvt_pk_f32_fp8_e32 v[158:159], v148
	v_cvt_pk_f32_fp8_sdwa v[154:155], v150 src0_sel:WORD_1
	v_pk_mul_f32 v[58:59], v[58:59], v[156:157]
	v_max_f32_e32 v152, v152, v152
	v_med3_f32 v152, v152, s35, v177
	v_mul_f32_e32 v152, 0xbfb8aa3b, v152
	v_max_f32_e32 v134, v158, v158
	v_exp_f32_e32 v158, v152
	v_med3_f32 v134, v134, s35, v177
	v_max_f32_e32 v153, v153, v153
	v_mul_f32_e32 v134, 0xbfb8aa3b, v134
	v_med3_f32 v153, v153, s35, v177
	v_exp_f32_e32 v152, v134
	v_add_f32_e32 v134, 1.0, v158
	v_mul_f32_e32 v153, 0xbfb8aa3b, v153
	v_rcp_f32_e32 v158, v134
	v_max_f32_e32 v134, v159, v159
	v_exp_f32_e32 v159, v153
	v_med3_f32 v134, v134, s35, v177
	v_max_f32_e32 v154, v154, v154
	v_mul_f32_e32 v134, 0xbfb8aa3b, v134
	v_med3_f32 v154, v154, s35, v177
	v_exp_f32_e32 v153, v134
	v_add_f32_e32 v134, 1.0, v159
	v_mul_f32_e32 v154, 0xbfb8aa3b, v154
	v_rcp_f32_e32 v159, v134
	v_max_f32_e32 v134, v160, v160
	v_exp_f32_e32 v160, v154
	v_cvt_pk_f32_fp8_e32 v[156:157], v151
	v_max_f32_e32 v155, v155, v155
	v_med3_f32 v134, v134, s35, v177
	v_med3_f32 v155, v155, s35, v177
	v_mul_f32_e32 v134, 0xbfb8aa3b, v134
	v_mul_f32_e32 v155, 0xbfb8aa3b, v155
	v_pk_add_f32 v[152:153], v[152:153], 1.0 op_sel_hi:[1,0]
	v_exp_f32_e32 v154, v134
	v_add_f32_e32 v134, 1.0, v160
	v_max_f32_e32 v160, v161, v161
	v_exp_f32_e32 v161, v155
	v_pk_mul_f32 v[152:153], v[158:159], v[152:153]
	v_cvt_pk_f32_fp8_e32 v[162:163], v149
	v_pk_mul_f32 v[46:47], v[46:47], v[152:153]
	v_max_f32_e32 v152, v156, v156
	v_med3_f32 v152, v152, s35, v177
	v_med3_f32 v160, v160, s35, v177
	v_mul_f32_e32 v152, 0xbfb8aa3b, v152
	v_mul_f32_e32 v155, 0xbfb8aa3b, v160
	v_rcp_f32_e32 v160, v134
	v_add_f32_e32 v134, 1.0, v161
	v_exp_f32_e32 v153, v152
	v_exp_f32_e32 v155, v155
	v_rcp_f32_e32 v161, v134
	v_max_f32_e32 v134, v162, v162
	v_med3_f32 v134, v134, s35, v177
	v_mul_f32_e32 v134, 0xbfb8aa3b, v134
	v_exp_f32_e32 v152, v134
	v_add_f32_e32 v134, 1.0, v153
	v_max_f32_e32 v153, v157, v157
	v_pk_add_f32 v[154:155], v[154:155], 1.0 op_sel_hi:[1,0]
	v_med3_f32 v153, v153, s35, v177
	v_pk_mul_f32 v[154:155], v[160:161], v[154:155]
	v_mul_f32_e32 v153, 0xbfb8aa3b, v153
	v_pk_mul_f32 v[48:49], v[48:49], v[154:155]
	v_exp_f32_e32 v155, v153
	v_cvt_pk_f32_fp8_sdwa v[150:151], v151 src0_sel:WORD_1
	v_cvt_pk_f32_fp8_sdwa v[148:149], v149 src0_sel:WORD_1
	v_rcp_f32_e32 v154, v134
	v_max_f32_e32 v134, v163, v163
	v_med3_f32 v134, v134, s35, v177
	v_mul_f32_e32 v134, 0xbfb8aa3b, v134
	v_exp_f32_e32 v153, v134
	v_add_f32_e32 v134, 1.0, v155
	v_rcp_f32_e32 v155, v134
	v_max_f32_e32 v134, v148, v148
	v_max_f32_e32 v148, v150, v150
	v_med3_f32 v148, v148, s35, v177
	v_mul_f32_e32 v148, 0xbfb8aa3b, v148
	v_exp_f32_e32 v150, v148
	v_med3_f32 v134, v134, s35, v177
	v_mul_f32_e32 v134, 0xbfb8aa3b, v134
	v_exp_f32_e32 v148, v134
	v_add_f32_e32 v134, 1.0, v150
	v_max_f32_e32 v150, v151, v151
	v_med3_f32 v150, v150, s35, v177
	v_mul_f32_e32 v150, 0xbfb8aa3b, v150
	v_exp_f32_e32 v151, v150
	v_max_f32_e32 v149, v149, v149
	v_med3_f32 v149, v149, s35, v177
	v_mul_f32_e32 v149, 0xbfb8aa3b, v149
	v_exp_f32_e32 v149, v149
	v_rcp_f32_e32 v150, v134
	v_add_f32_e32 v134, 1.0, v151
	v_rcp_f32_e32 v151, v134
	v_pk_add_f32 v[148:149], v[148:149], 1.0 op_sel_hi:[1,0]
	v_pk_add_f32 v[152:153], v[152:153], 1.0 op_sel_hi:[1,0]
	s_waitcnt vmcnt(4)
	v_cvt_pk_f32_fp8_sdwa v[156:157], v144 src0_sel:WORD_1
	v_pk_mul_f32 v[148:149], v[150:151], v[148:149]
	v_pk_mul_f32 v[152:153], v[154:155], v[152:153]
	v_pk_mul_f32 v[36:37], v[36:37], v[148:149]
	v_cvt_pk_f32_fp8_e32 v[148:149], v146
	v_cvt_pk_f32_fp8_e32 v[154:155], v144
	v_cvt_pk_f32_fp8_sdwa v[150:151], v146 src0_sel:WORD_1
	v_pk_mul_f32 v[34:35], v[34:35], v[152:153]
	v_max_f32_e32 v148, v148, v148
	v_med3_f32 v148, v148, s35, v177
	v_mul_f32_e32 v148, 0xbfb8aa3b, v148
	v_max_f32_e32 v134, v154, v154
	v_exp_f32_e32 v154, v148
	v_med3_f32 v134, v134, s35, v177
	v_max_f32_e32 v149, v149, v149
	v_mul_f32_e32 v134, 0xbfb8aa3b, v134
	v_med3_f32 v149, v149, s35, v177
	v_exp_f32_e32 v148, v134
	v_add_f32_e32 v134, 1.0, v154
	v_mul_f32_e32 v149, 0xbfb8aa3b, v149
	v_rcp_f32_e32 v154, v134
	v_max_f32_e32 v134, v155, v155
	v_exp_f32_e32 v155, v149
	v_med3_f32 v134, v134, s35, v177
	v_max_f32_e32 v150, v150, v150
	v_mul_f32_e32 v134, 0xbfb8aa3b, v134
	v_med3_f32 v150, v150, s35, v177
	v_exp_f32_e32 v149, v134
	v_add_f32_e32 v134, 1.0, v155
	v_mul_f32_e32 v150, 0xbfb8aa3b, v150
	v_rcp_f32_e32 v155, v134
	v_max_f32_e32 v134, v156, v156
	v_exp_f32_e32 v156, v150
	v_cvt_pk_f32_fp8_e32 v[152:153], v147
	v_max_f32_e32 v151, v151, v151
	v_med3_f32 v134, v134, s35, v177
	v_med3_f32 v151, v151, s35, v177
	v_mul_f32_e32 v134, 0xbfb8aa3b, v134
	v_mul_f32_e32 v151, 0xbfb8aa3b, v151
	v_pk_add_f32 v[148:149], v[148:149], 1.0 op_sel_hi:[1,0]
	v_exp_f32_e32 v150, v134
	v_add_f32_e32 v134, 1.0, v156
	v_max_f32_e32 v156, v157, v157
	v_exp_f32_e32 v157, v151
	v_pk_mul_f32 v[148:149], v[154:155], v[148:149]
	v_cvt_pk_f32_fp8_e32 v[158:159], v145
	v_pk_mul_f32 v[22:23], v[22:23], v[148:149]
	v_max_f32_e32 v148, v152, v152
	v_med3_f32 v148, v148, s35, v177
	v_med3_f32 v156, v156, s35, v177
	v_mul_f32_e32 v148, 0xbfb8aa3b, v148
	v_mul_f32_e32 v151, 0xbfb8aa3b, v156
	v_rcp_f32_e32 v156, v134
	v_add_f32_e32 v134, 1.0, v157
	v_exp_f32_e32 v149, v148
	v_exp_f32_e32 v151, v151
	v_rcp_f32_e32 v157, v134
	v_max_f32_e32 v134, v158, v158
	v_med3_f32 v134, v134, s35, v177
	v_mul_f32_e32 v134, 0xbfb8aa3b, v134
	v_exp_f32_e32 v148, v134
	v_add_f32_e32 v134, 1.0, v149
	v_max_f32_e32 v149, v153, v153
	v_pk_add_f32 v[150:151], v[150:151], 1.0 op_sel_hi:[1,0]
	v_med3_f32 v149, v149, s35, v177
	v_pk_mul_f32 v[150:151], v[156:157], v[150:151]
	v_mul_f32_e32 v149, 0xbfb8aa3b, v149
	v_pk_mul_f32 v[24:25], v[24:25], v[150:151]
	v_exp_f32_e32 v151, v149
	v_cvt_pk_f32_fp8_sdwa v[146:147], v147 src0_sel:WORD_1
	v_cvt_pk_f32_fp8_sdwa v[144:145], v145 src0_sel:WORD_1
	v_rcp_f32_e32 v150, v134
	v_max_f32_e32 v134, v159, v159
	v_med3_f32 v134, v134, s35, v177
	v_mul_f32_e32 v134, 0xbfb8aa3b, v134
	v_exp_f32_e32 v149, v134
	v_add_f32_e32 v134, 1.0, v151
	v_rcp_f32_e32 v151, v134
	v_max_f32_e32 v134, v144, v144
	v_max_f32_e32 v144, v146, v146
	v_med3_f32 v144, v144, s35, v177
	v_mul_f32_e32 v144, 0xbfb8aa3b, v144
	v_exp_f32_e32 v146, v144
	v_med3_f32 v134, v134, s35, v177
	v_mul_f32_e32 v134, 0xbfb8aa3b, v134
	v_exp_f32_e32 v144, v134
	v_add_f32_e32 v134, 1.0, v146
	v_max_f32_e32 v146, v147, v147
	v_med3_f32 v146, v146, s35, v177
	v_mul_f32_e32 v146, 0xbfb8aa3b, v146
	v_exp_f32_e32 v147, v146
	v_max_f32_e32 v145, v145, v145
	v_med3_f32 v145, v145, s35, v177
	v_mul_f32_e32 v145, 0xbfb8aa3b, v145
	v_exp_f32_e32 v145, v145
	v_rcp_f32_e32 v146, v134
	v_add_f32_e32 v134, 1.0, v147
	v_rcp_f32_e32 v147, v134
	v_pk_add_f32 v[144:145], v[144:145], 1.0 op_sel_hi:[1,0]
	v_pk_add_f32 v[148:149], v[148:149], 1.0 op_sel_hi:[1,0]
	s_waitcnt vmcnt(2)
	v_cvt_pk_f32_fp8_sdwa v[152:153], v140 src0_sel:WORD_1
	v_pk_mul_f32 v[144:145], v[146:147], v[144:145]
	v_pk_mul_f32 v[148:149], v[150:151], v[148:149]
	v_pk_mul_f32 v[20:21], v[20:21], v[144:145]
	v_cvt_pk_f32_fp8_e32 v[144:145], v142
	v_cvt_pk_f32_fp8_e32 v[150:151], v140
	v_cvt_pk_f32_fp8_sdwa v[146:147], v142 src0_sel:WORD_1
	v_pk_mul_f32 v[18:19], v[18:19], v[148:149]
	v_max_f32_e32 v144, v144, v144
	v_med3_f32 v144, v144, s35, v177
	v_mul_f32_e32 v144, 0xbfb8aa3b, v144
	v_max_f32_e32 v134, v150, v150
	v_exp_f32_e32 v150, v144
	v_med3_f32 v134, v134, s35, v177
	v_max_f32_e32 v145, v145, v145
	v_mul_f32_e32 v134, 0xbfb8aa3b, v134
	v_med3_f32 v145, v145, s35, v177
	v_exp_f32_e32 v144, v134
	v_add_f32_e32 v134, 1.0, v150
	v_mul_f32_e32 v145, 0xbfb8aa3b, v145
	v_rcp_f32_e32 v150, v134
	v_max_f32_e32 v134, v151, v151
	v_exp_f32_e32 v151, v145
	v_med3_f32 v134, v134, s35, v177
	v_max_f32_e32 v146, v146, v146
	v_mul_f32_e32 v134, 0xbfb8aa3b, v134
	v_med3_f32 v146, v146, s35, v177
	v_exp_f32_e32 v145, v134
	v_add_f32_e32 v134, 1.0, v151
	v_mul_f32_e32 v146, 0xbfb8aa3b, v146
	v_rcp_f32_e32 v151, v134
	v_max_f32_e32 v134, v152, v152
	v_exp_f32_e32 v152, v146
	v_cvt_pk_f32_fp8_e32 v[148:149], v143
	v_max_f32_e32 v147, v147, v147
	v_med3_f32 v134, v134, s35, v177
	v_med3_f32 v147, v147, s35, v177
	v_mul_f32_e32 v134, 0xbfb8aa3b, v134
	v_mul_f32_e32 v147, 0xbfb8aa3b, v147
	v_pk_add_f32 v[144:145], v[144:145], 1.0 op_sel_hi:[1,0]
	v_exp_f32_e32 v146, v134
	v_add_f32_e32 v134, 1.0, v152
	v_max_f32_e32 v152, v153, v153
	v_exp_f32_e32 v153, v147
	v_pk_mul_f32 v[144:145], v[150:151], v[144:145]
	v_cvt_pk_f32_fp8_e32 v[154:155], v141
	v_pk_mul_f32 v[14:15], v[14:15], v[144:145]
	v_max_f32_e32 v144, v148, v148
	v_med3_f32 v144, v144, s35, v177
	v_med3_f32 v152, v152, s35, v177
	v_mul_f32_e32 v144, 0xbfb8aa3b, v144
	v_mul_f32_e32 v147, 0xbfb8aa3b, v152
	v_rcp_f32_e32 v152, v134
	v_add_f32_e32 v134, 1.0, v153
	v_exp_f32_e32 v145, v144
	v_exp_f32_e32 v147, v147
	v_rcp_f32_e32 v153, v134
	v_max_f32_e32 v134, v154, v154
	v_med3_f32 v134, v134, s35, v177
	v_mul_f32_e32 v134, 0xbfb8aa3b, v134
	v_exp_f32_e32 v144, v134
	v_add_f32_e32 v134, 1.0, v145
	v_max_f32_e32 v145, v149, v149
	v_pk_add_f32 v[146:147], v[146:147], 1.0 op_sel_hi:[1,0]
	v_med3_f32 v145, v145, s35, v177
	v_pk_mul_f32 v[146:147], v[152:153], v[146:147]
	v_mul_f32_e32 v145, 0xbfb8aa3b, v145
	v_pk_mul_f32 v[16:17], v[16:17], v[146:147]
	v_exp_f32_e32 v147, v145
	v_cvt_pk_f32_fp8_sdwa v[142:143], v143 src0_sel:WORD_1
	v_cvt_pk_f32_fp8_sdwa v[140:141], v141 src0_sel:WORD_1
	v_rcp_f32_e32 v146, v134
	v_max_f32_e32 v134, v155, v155
	v_med3_f32 v134, v134, s35, v177
	v_mul_f32_e32 v134, 0xbfb8aa3b, v134
	v_exp_f32_e32 v145, v134
	v_add_f32_e32 v134, 1.0, v147
	v_rcp_f32_e32 v147, v134
	v_max_f32_e32 v134, v140, v140
	v_max_f32_e32 v140, v142, v142
	v_med3_f32 v140, v140, s35, v177
	v_mul_f32_e32 v140, 0xbfb8aa3b, v140
	v_exp_f32_e32 v142, v140
	v_med3_f32 v134, v134, s35, v177
	v_mul_f32_e32 v134, 0xbfb8aa3b, v134
	v_exp_f32_e32 v140, v134
	v_add_f32_e32 v134, 1.0, v142
	v_max_f32_e32 v142, v143, v143
	v_med3_f32 v142, v142, s35, v177
	v_mul_f32_e32 v142, 0xbfb8aa3b, v142
	v_exp_f32_e32 v143, v142
	v_max_f32_e32 v141, v141, v141
	v_med3_f32 v141, v141, s35, v177
	v_mul_f32_e32 v141, 0xbfb8aa3b, v141
	v_exp_f32_e32 v141, v141
	v_rcp_f32_e32 v142, v134
	v_add_f32_e32 v134, 1.0, v143
	v_rcp_f32_e32 v143, v134
	v_pk_add_f32 v[140:141], v[140:141], 1.0 op_sel_hi:[1,0]
	v_pk_add_f32 v[144:145], v[144:145], 1.0 op_sel_hi:[1,0]
	s_waitcnt vmcnt(0)
	v_cvt_pk_f32_fp8_sdwa v[148:149], v136 src0_sel:WORD_1
	v_pk_mul_f32 v[140:141], v[142:143], v[140:141]
	v_pk_mul_f32 v[144:145], v[146:147], v[144:145]
	v_pk_mul_f32 v[12:13], v[12:13], v[140:141]
	v_cvt_pk_f32_fp8_e32 v[140:141], v138
	v_cvt_pk_f32_fp8_e32 v[146:147], v136
	v_cvt_pk_f32_fp8_sdwa v[142:143], v138 src0_sel:WORD_1
	v_pk_mul_f32 v[10:11], v[10:11], v[144:145]
	v_max_f32_e32 v140, v140, v140
	v_med3_f32 v140, v140, s35, v177
	v_mul_f32_e32 v140, 0xbfb8aa3b, v140
	v_max_f32_e32 v134, v146, v146
	v_exp_f32_e32 v146, v140
	v_med3_f32 v134, v134, s35, v177
	v_max_f32_e32 v141, v141, v141
	v_mul_f32_e32 v134, 0xbfb8aa3b, v134
	v_med3_f32 v141, v141, s35, v177
	v_exp_f32_e32 v140, v134
	v_add_f32_e32 v134, 1.0, v146
	v_mul_f32_e32 v141, 0xbfb8aa3b, v141
	v_rcp_f32_e32 v146, v134
	v_max_f32_e32 v134, v147, v147
	v_exp_f32_e32 v147, v141
	v_med3_f32 v134, v134, s35, v177
	v_max_f32_e32 v142, v142, v142
	v_mul_f32_e32 v134, 0xbfb8aa3b, v134
	v_med3_f32 v142, v142, s35, v177
	v_exp_f32_e32 v141, v134
	v_add_f32_e32 v134, 1.0, v147
	v_mul_f32_e32 v142, 0xbfb8aa3b, v142
	v_rcp_f32_e32 v147, v134
	v_max_f32_e32 v134, v148, v148
	v_exp_f32_e32 v148, v142
	v_cvt_pk_f32_fp8_e32 v[144:145], v139
	v_max_f32_e32 v143, v143, v143
	v_med3_f32 v134, v134, s35, v177
	v_med3_f32 v143, v143, s35, v177
	v_mul_f32_e32 v134, 0xbfb8aa3b, v134
	v_mul_f32_e32 v143, 0xbfb8aa3b, v143
	v_pk_add_f32 v[140:141], v[140:141], 1.0 op_sel_hi:[1,0]
	v_exp_f32_e32 v142, v134
	v_add_f32_e32 v134, 1.0, v148
	v_max_f32_e32 v148, v149, v149
	v_exp_f32_e32 v149, v143
	v_pk_mul_f32 v[140:141], v[146:147], v[140:141]
	v_cvt_pk_f32_fp8_e32 v[150:151], v137
	v_pk_mul_f32 v[6:7], v[6:7], v[140:141]
	v_max_f32_e32 v140, v144, v144
	v_med3_f32 v140, v140, s35, v177
	v_med3_f32 v148, v148, s35, v177
	v_mul_f32_e32 v140, 0xbfb8aa3b, v140
	v_mul_f32_e32 v143, 0xbfb8aa3b, v148
	v_rcp_f32_e32 v148, v134
	v_add_f32_e32 v134, 1.0, v149
	v_exp_f32_e32 v141, v140
	v_exp_f32_e32 v143, v143
	v_rcp_f32_e32 v149, v134
	v_max_f32_e32 v134, v150, v150
	v_med3_f32 v134, v134, s35, v177
	v_mul_f32_e32 v134, 0xbfb8aa3b, v134
	v_exp_f32_e32 v140, v134
	v_add_f32_e32 v134, 1.0, v141
	v_max_f32_e32 v141, v145, v145
	v_pk_add_f32 v[142:143], v[142:143], 1.0 op_sel_hi:[1,0]
	v_med3_f32 v141, v141, s35, v177
	v_pk_mul_f32 v[142:143], v[148:149], v[142:143]
	v_mul_f32_e32 v141, 0xbfb8aa3b, v141
	v_pk_mul_f32 v[8:9], v[8:9], v[142:143]
	v_exp_f32_e32 v143, v141
	v_cvt_pk_f32_fp8_sdwa v[138:139], v139 src0_sel:WORD_1
	v_cvt_pk_f32_fp8_sdwa v[136:137], v137 src0_sel:WORD_1
	v_rcp_f32_e32 v142, v134
	v_max_f32_e32 v134, v151, v151
	v_med3_f32 v134, v134, s35, v177
	v_mul_f32_e32 v134, 0xbfb8aa3b, v134
	v_exp_f32_e32 v141, v134
	v_add_f32_e32 v134, 1.0, v143
	v_rcp_f32_e32 v143, v134
	v_max_f32_e32 v134, v136, v136
	v_max_f32_e32 v136, v138, v138
	v_med3_f32 v136, v136, s35, v177
	v_mul_f32_e32 v136, 0xbfb8aa3b, v136
	v_exp_f32_e32 v138, v136
	v_med3_f32 v134, v134, s35, v177
	v_mul_f32_e32 v134, 0xbfb8aa3b, v134
	v_exp_f32_e32 v136, v134
	v_add_f32_e32 v134, 1.0, v138
	v_max_f32_e32 v138, v139, v139
	v_med3_f32 v138, v138, s35, v177
	v_mul_f32_e32 v138, 0xbfb8aa3b, v138
	v_exp_f32_e32 v139, v138
	v_max_f32_e32 v137, v137, v137
	v_med3_f32 v137, v137, s35, v177
	v_mul_f32_e32 v137, 0xbfb8aa3b, v137
	v_exp_f32_e32 v137, v137
	v_rcp_f32_e32 v138, v134
	v_add_f32_e32 v134, 1.0, v139
	v_rcp_f32_e32 v139, v134
	v_pk_add_f32 v[136:137], v[136:137], 1.0 op_sel_hi:[1,0]
	v_pk_add_f32 v[140:141], v[140:141], 1.0 op_sel_hi:[1,0]
	v_pk_mul_f32 v[136:137], v[138:139], v[136:137]
	v_pk_mul_f32 v[140:141], v[142:143], v[140:141]
	v_pk_mul_f32 v[4:5], v[4:5], v[136:137]
	v_pk_mul_f32 v[2:3], v[2:3], v[140:141]
	s_nop 0
